# adds write-through (sc1) on the P0 prologue and P1 in-proj epilogue stores so the seam L2 write-back has less dirty data
# speedup vs baseline: 1.0043x; 1.0004x over previous
; __device__ __forceinline__ void p0_prologue(Ctx& X) {
;     ...
;     for (int m = gw; m < T; m += 4 * NGW) {
;         const f32x4* wr_ = (const f32x4*)XP_ln_mix_w(X) + lane;
;         f32x4 v[4][8]; float s[4] = {0.f, 0.f, 0.f, 0.f};
; #pragma unroll
;         for (int r = 0; r < 4; ++r) { const int mm = (m + r * NGW < T) ? m + r * NGW : m; const f32x4* xr = (const f32x4*)(XP_x(X) + (size_t)mm * D) + lane;
; #pragma unroll
;             for (int j = 0; j < 8; ++j) v[r][j] = __builtin_nontemporal_load(&xr[64 * j]); }
; #pragma unroll
;         for (int r = 0; r < 4; ++r)
; #pragma unroll
;             for (int j = 0; j < 8; ++j) s[r] += (v[r][j].x * v[r][j].x + v[r][j].y * v[r][j].y) + (v[r][j].z * v[r][j].z + v[r][j].w * v[r][j].w);
;         f32x4 w[8];
; #pragma unroll
;         for (int j = 0; j < 8; ++j) w[j] = wr_[64 * j];
; #pragma unroll
;         for (int r = 0; r < 4; ++r) { const int mm = m + r * NGW; if (mm >= T) break;
;             const float rstd = rsqrtf(wave_sum(s[r]) * (1.f / D) + EPS);
.LBB0_13:
	global_load_dwordx4 v[22:25], v[176:177], off offset:-4096 nt
	global_load_dwordx4 v[114:117], v[176:177], off offset:-3072 nt
	global_load_dwordx4 v[110:113], v[176:177], off offset:-2048 nt
	global_load_dwordx4 v[98:101], v[176:177], off offset:1024 nt
	global_load_dwordx4 v[118:121], v[176:177], off nt
	global_load_dwordx4 v[122:125], v[176:177], off offset:-1024 nt
	global_load_dwordx4 v[106:109], v[176:177], off offset:2048 nt
	global_load_dwordx4 v[94:97], v[176:177], off offset:3072 nt
	global_load_dwordx4 v[2:5], v[160:161], off
	global_load_dwordx4 v[18:21], v[160:161], off offset:1024
	global_load_dwordx4 v[14:17], v[160:161], off offset:2048
	global_load_dwordx4 v[10:13], v[160:161], off offset:3072
	global_load_dwordx4 v[6:9], v[168:169], off
	s_add_i32 s15, s24, s38
	s_cmpk_lt_i32 s15, 0x2000
	s_cselect_b32 s2, s15, s38
	s_ashr_i32 s3, s2, 31
	s_add_i32 s18, s5, s38
	s_lshl_b64 s[2:3], s[2:3], 13
	s_cmpk_lt_i32 s18, 0x2000
	s_cselect_b64 s[20:21], -1, 0
	v_lshl_add_u64 v[180:181], v[174:175], 0, v[172:173]
	v_lshl_add_u64 v[26:27], v[158:159], 0, s[2:3]
	s_and_b64 s[2:3], s[20:21], exec
	v_add_co_u32_e32 v190, vcc, s25, v180
	s_cselect_b32 s2, s18, s38
	s_nop 0
	v_addc_co_u32_e32 v191, vcc, 0, v181, vcc
	s_ashr_i32 s3, s2, 31
	global_load_dwordx4 v[154:157], v[26:27], off nt
	global_load_dwordx4 v[150:153], v[26:27], off offset:1024 nt
	global_load_dwordx4 v[146:149], v[26:27], off offset:2048 nt
	global_load_dwordx4 v[142:145], v[26:27], off offset:3072 nt
	v_add_co_u32_e32 v26, vcc, s22, v26
	s_lshl_b64 s[2:3], s[2:3], 13
	s_nop 0
	v_addc_co_u32_e32 v27, vcc, 0, v27, vcc
	s_add_i32 s14, s11, s38
	s_cmpk_lt_i32 s14, 0x2000
	s_cselect_b64 s[16:17], -1, 0
	global_load_dwordx4 v[134:137], v[26:27], off nt
	global_load_dwordx4 v[126:129], v[26:27], off offset:1024 nt
	s_waitcnt vmcnt(18)
	v_mov_b32_e32 v30, v23
	s_waitcnt vmcnt(17)
	v_mov_b32_e32 v31, v115
	s_waitcnt vmcnt(16)
	v_pk_mul_f32 v[32:33], v[112:113], v[112:113]
	v_pk_mul_f32 v[34:35], v[110:111], v[110:111]
	s_waitcnt vmcnt(15)
	v_pk_mul_f32 v[36:37], v[100:101], v[100:101]
	v_pk_mul_f32 v[38:39], v[98:99], v[98:99]
	v_mov_b32_e32 v42, v25
	v_mov_b32_e32 v43, v117
	v_mov_b32_e32 v28, v22
	v_mov_b32_e32 v29, v114
	v_mov_b32_e32 v40, v24
	v_mov_b32_e32 v41, v116
	v_pk_mov_b32 v[52:53], v[34:35], v[32:33] op_sel:[1,0]
	v_mov_b32_e32 v35, v33
	v_pk_mov_b32 v[32:33], v[38:39], v[36:37] op_sel:[1,0]
	v_mov_b32_e32 v39, v37
	v_pk_mul_f32 v[30:31], v[30:31], v[30:31]
	v_pk_mul_f32 v[36:37], v[42:43], v[42:43]
	v_pk_fma_f32 v[28:29], v[28:29], v[28:29], v[30:31]
	v_pk_fma_f32 v[30:31], v[40:41], v[40:41], v[36:37]
	s_waitcnt vmcnt(13)
	v_mul_f32_e32 v44, v123, v123
	v_mul_f32_e32 v46, v125, v125
	v_pk_add_f32 v[34:35], v[52:53], v[34:35]
	v_pk_add_f32 v[28:29], v[28:29], v[30:31]
	v_mul_f32_e32 v51, v120, v120
	v_mul_f32_e32 v54, v121, v121
	v_mul_f32_e32 v57, v119, v119
	v_mul_f32_e32 v58, v118, v118
	v_pk_fma_f32 v[42:43], v[122:123], v[122:123], v[44:45] op_sel_hi:[1,1,0]
	v_pk_fma_f32 v[44:45], v[124:125], v[124:125], v[46:47] op_sel_hi:[1,1,0]
	v_pk_add_f32 v[34:35], v[34:35], v[34:35] op_sel:[0,1] op_sel_hi:[1,0]
	v_pk_add_f32 v[28:29], v[28:29], v[28:29] op_sel:[0,1] op_sel_hi:[1,0]
	v_mov_b32_e32 v43, v51
	v_mov_b32_e32 v45, v54
	v_mov_b32_e32 v35, v57
	v_mov_b32_e32 v29, v58
	v_pk_add_f32 v[30:31], v[42:43], v[44:45]
	v_pk_add_f32 v[28:29], v[28:29], v[34:35]
	s_waitcnt vmcnt(12)
	v_mul_f32_e32 v48, v107, v107
	v_mul_f32_e32 v50, v109, v109
	v_pk_add_f32 v[32:33], v[32:33], v[38:39]
	v_pk_add_f32 v[28:29], v[28:29], v[30:31]
	s_waitcnt vmcnt(11)
	v_mul_f32_e32 v55, v96, v96
	v_mul_f32_e32 v56, v97, v97
	v_mul_f32_e32 v59, v95, v95
	v_mul_f32_e32 v60, v94, v94
	v_pk_fma_f32 v[46:47], v[106:107], v[106:107], v[48:49] op_sel_hi:[1,1,0]
	v_pk_fma_f32 v[48:49], v[108:109], v[108:109], v[50:51] op_sel_hi:[1,1,0]
	v_pk_add_f32 v[32:33], v[32:33], v[32:33] op_sel:[0,1] op_sel_hi:[1,0]
	v_pk_add_f32 v[28:29], v[28:29], v[28:29] op_sel:[0,1] op_sel_hi:[1,0]
	v_mov_b32_e32 v47, v55
	v_mov_b32_e32 v49, v56
	v_mov_b32_e32 v33, v59
	v_mov_b32_e32 v29, v60
	v_pk_add_f32 v[36:37], v[46:47], v[48:49]
	v_pk_add_f32 v[28:29], v[28:29], v[32:33]
	s_nop 0
	v_pk_add_f32 v[28:29], v[28:29], v[36:37]
	s_nop 0
	v_add_f32_e32 v28, v28, v29
	ds_bpermute_b32 v29, v182, v28
	s_waitcnt lgkmcnt(0)
	v_add_f32_e32 v28, v28, v29
	ds_bpermute_b32 v29, v183, v28
	s_waitcnt lgkmcnt(0)
	v_add_f32_e32 v28, v28, v29
	ds_bpermute_b32 v29, v184, v28
	s_waitcnt lgkmcnt(0)
	v_add_f32_e32 v30, v28, v29
	ds_bpermute_b32 v31, v185, v30
	v_lshl_add_u64 v[28:29], v[158:159], 0, s[2:3]
	s_and_b64 s[2:3], s[16:17], exec
	s_cselect_b32 s2, s14, s38
	s_ashr_i32 s3, s2, 31
	s_waitcnt lgkmcnt(0)
	v_add_f32_e32 v32, v30, v31
	ds_bpermute_b32 v33, v186, v32
	v_add_co_u32_e32 v30, vcc, s22, v28
	s_lshl_b64 s[2:3], s[2:3], 13
	s_nop 0
	v_addc_co_u32_e32 v31, vcc, 0, v29, vcc
	s_waitcnt lgkmcnt(0)
	v_add_f32_e32 v34, v32, v33
	ds_bpermute_b32 v35, v187, v34
	v_lshl_add_u64 v[32:33], v[158:159], 0, s[2:3]
	s_cmpk_gt_i32 s15, 0x1fff
	s_waitcnt lgkmcnt(0)
	v_add_f32_e32 v34, v34, v35
	v_fmamk_f32 v34, v34, 0x3a000000, v188
	v_mul_f32_e32 v35, 0x4b800000, v34
	v_cmp_gt_f32_e32 vcc, s23, v34
	s_nop 1
	v_cndmask_b32_e32 v34, v34, v35, vcc
	v_rsq_f32_e32 v36, v34
	v_add_co_u32_e64 v34, s[2:3], s22, v32
	v_mul_f32_e32 v37, 0x45800000, v36
	v_cndmask_b32_e32 v189, v36, v37, vcc
	v_mul_f32_e32 v22, v22, v189
	v_mul_f32_e32 v23, v23, v189
	v_mul_f32_e32 v24, v24, v189
	v_mul_f32_e32 v25, v25, v189
	v_addc_co_u32_e64 v35, s[2:3], 0, v33, s[2:3]
	s_waitcnt vmcnt(10)
; __device__ __forceinline__ unsigned pk_bf16(float lo, float hi) { unsigned r; asm("v_cvt_pk_bf16_f32 %0, %1, %2" : "=v"(r) : "v"(lo), "v"(hi)); return r; }
; __device__ __forceinline__ void p0_prologue(Ctx& X) {
;     ...
;         f32x4 w[8];
; #pragma unroll
;         for (int j = 0; j < 8; ++j) w[j] = wr_[64 * j];
; #pragma unroll
;         for (int r = 0; r < 4; ++r) { const int mm = m + r * NGW; if (mm >= T) break;
;             const float rstd = rsqrtf(wave_sum(s[r]) * (1.f / D) + EPS);
;             bf16* o8 = XP_U(X) + (size_t)(lane >> 4) * PANE_A + (size_t)mm * 64 + 4 * (lane & 15);
; #pragma unroll
;             for (int j = 0; j < 8; ++j) { u32x2 o; o.x = pk_bf16(v[r][j].x * rstd * w[j].x, v[r][j].y * rstd * w[j].y); o.y = pk_bf16(v[r][j].z * rstd * w[j].z, v[r][j].w * rstd * w[j].w); *(u32x2*)(o8 + (size_t)(4 * j) * PANE_A) = o; } }
	v_mul_f32_e32 v22, v2, v22
	v_mul_f32_e32 v23, v3, v23
	v_mul_f32_e32 v24, v4, v24
	v_mul_f32_e32 v25, v5, v25
	v_cvt_pk_bf16_f32 v192, v22, v23
	v_cvt_pk_bf16_f32 v193, v24, v25
	global_load_dwordx4 v[138:141], v[26:27], off offset:2048 nt
	global_load_dwordx4 v[130:133], v[26:27], off offset:3072 nt
	global_load_dwordx4 v[102:105], v[28:29], off nt
	global_load_dwordx4 v[90:93], v[28:29], off offset:1024 nt
	global_load_dwordx4 v[86:89], v[28:29], off offset:2048 nt
	global_load_dwordx4 v[82:85], v[28:29], off offset:3072 nt
	global_load_dwordx4 v[38:41], v[166:167], off
	global_load_dwordx4 v[78:81], v[30:31], off nt
	global_load_dwordx4 v[74:77], v[30:31], off offset:1024 nt
	global_load_dwordx4 v[70:73], v[30:31], off offset:2048 nt
	global_load_dwordx4 v[66:69], v[30:31], off offset:3072 nt
	global_load_dwordx4 v[62:65], v[32:33], off nt
	global_load_dwordx4 v[58:61], v[32:33], off offset:1024 nt
	global_load_dwordx4 v[54:57], v[32:33], off offset:2048 nt
	global_load_dwordx4 v[50:53], v[32:33], off offset:3072 nt
	global_load_dwordx4 v[46:49], v[34:35], off nt
	global_load_dwordx4 v[42:45], v[34:35], off offset:1024 nt
	s_nop 0
	global_load_dwordx4 v[30:33], v[34:35], off offset:2048 nt
	global_load_dwordx4 v[22:25], v[34:35], off offset:3072 nt
	global_load_dwordx4 v[26:29], v[162:163], off
	s_nop 0
	global_load_dwordx4 v[34:37], v[164:165], off
	v_mul_f32_e32 v114, v114, v189
	v_mul_f32_e32 v115, v115, v189
	v_mul_f32_e32 v116, v116, v189
	v_mul_f32_e32 v117, v117, v189
	s_waitcnt vmcnt(30)
	v_mul_f32_e32 v114, v18, v114
	v_mul_f32_e32 v115, v19, v115
	v_cvt_pk_bf16_f32 v114, v114, v115
	v_mul_f32_e32 v115, v20, v116
	v_mul_f32_e32 v116, v21, v117
	v_mul_f32_e32 v110, v110, v189
	v_mul_f32_e32 v111, v111, v189
	v_cvt_pk_bf16_f32 v115, v115, v116
	v_add_co_u32_e32 v116, vcc, s26, v180
	v_mul_f32_e32 v112, v112, v189
	v_mul_f32_e32 v113, v113, v189
	s_waitcnt vmcnt(29)
	v_mul_f32_e32 v110, v14, v110
	v_mul_f32_e32 v111, v15, v111
	v_addc_co_u32_e32 v117, vcc, 0, v181, vcc
	v_cvt_pk_bf16_f32 v110, v110, v111
	v_mul_f32_e32 v111, v16, v112
	v_mul_f32_e32 v112, v17, v113
	v_cvt_pk_bf16_f32 v111, v111, v112
	v_add_co_u32_e32 v112, vcc, s27, v180
	v_mul_f32_e32 v98, v98, v189
	s_nop 0
	v_addc_co_u32_e32 v113, vcc, 0, v181, vcc
	global_store_dwordx2 v[112:113], v[110:111], off sc1
	v_mul_f32_e32 v110, v122, v189
	v_mul_f32_e32 v111, v123, v189
	v_mul_f32_e32 v112, v124, v189
	v_mul_f32_e32 v113, v125, v189
	s_waitcnt vmcnt(29)
	v_mul_f32_e32 v110, v10, v110
	v_mul_f32_e32 v111, v11, v111
	v_cvt_pk_bf16_f32 v110, v110, v111
	v_mul_f32_e32 v111, v12, v112
	v_mul_f32_e32 v112, v13, v113
	v_cvt_pk_bf16_f32 v111, v111, v112
	v_add_co_u32_e32 v112, vcc, s28, v180
	v_mul_f32_e32 v99, v99, v189
	s_nop 0
	v_addc_co_u32_e32 v113, vcc, 0, v181, vcc
	global_store_dwordx2 v[112:113], v[110:111], off sc1
	v_mul_f32_e32 v110, v118, v189
	v_mul_f32_e32 v111, v119, v189
	v_mul_f32_e32 v112, v120, v189
	v_mul_f32_e32 v113, v121, v189
	s_waitcnt vmcnt(29)
	v_mul_f32_e32 v110, v6, v110
	v_mul_f32_e32 v111, v7, v111
	v_cvt_pk_bf16_f32 v110, v110, v111
	v_mul_f32_e32 v111, v8, v112
	v_mul_f32_e32 v112, v9, v113
	v_cvt_pk_bf16_f32 v111, v111, v112
	v_add_co_u32_e32 v112, vcc, s29, v180
	v_mul_f32_e32 v100, v100, v189
	v_mul_f32_e32 v101, v101, v189
	v_addc_co_u32_e32 v113, vcc, 0, v181, vcc
	v_mul_f32_e32 v94, v94, v189
	v_mul_f32_e32 v95, v95, v189
	v_mul_f32_e32 v96, v96, v189
	s_waitcnt vmcnt(16)
	v_mul_f32_e32 v98, v38, v98
	v_mul_f32_e32 v99, v39, v99
	v_cvt_pk_bf16_f32 v98, v98, v99
	v_mul_f32_e32 v99, v40, v100
	v_mul_f32_e32 v100, v41, v101
	v_cvt_pk_bf16_f32 v99, v99, v100
	v_add_co_u32_e32 v100, vcc, s30, v180
	v_mul_f32_e32 v97, v97, v189
	s_nop 0
	v_addc_co_u32_e32 v101, vcc, 0, v181, vcc
	global_store_dwordx2 v[100:101], v[98:99], off sc1
	v_mul_f32_e32 v98, v106, v189
	v_mul_f32_e32 v99, v107, v189
	v_mul_f32_e32 v100, v108, v189
	v_mul_f32_e32 v101, v109, v189
	s_waitcnt vmcnt(3)
	v_mul_f32_e32 v98, v34, v98
	v_mul_f32_e32 v99, v35, v99
	v_cvt_pk_bf16_f32 v98, v98, v99
	v_mul_f32_e32 v99, v36, v100
	v_mul_f32_e32 v100, v37, v101
	v_cvt_pk_bf16_f32 v99, v99, v100
	v_add_co_u32_e32 v100, vcc, s31, v180
	v_mul_f32_e32 v94, v26, v94
	v_mul_f32_e32 v95, v27, v95
	v_addc_co_u32_e32 v101, vcc, 0, v181, vcc
	v_cvt_pk_bf16_f32 v94, v94, v95
	v_mul_f32_e32 v95, v28, v96
	v_mul_f32_e32 v96, v29, v97
	v_cvt_pk_bf16_f32 v95, v95, v96
	v_add_co_u32_e32 v96, vcc, 0x5c00000, v180
	global_store_dwordx2 v[190:191], v[192:193], off sc1
	s_nop 0
	v_addc_co_u32_e32 v97, vcc, 0, v181, vcc
	global_store_dwordx2 v[116:117], v[114:115], off sc1
	global_store_dwordx2 v[112:113], v[110:111], off sc1
	global_store_dwordx2 v[100:101], v[98:99], off sc1
	global_store_dwordx2 v[96:97], v[94:95], off sc1
	s_cbranch_scc1 .LBB0_12
; __device__ __forceinline__ unsigned pk_bf16(float lo, float hi) { unsigned r; asm("v_cvt_pk_bf16_f32 %0, %1, %2" : "=v"(r) : "v"(lo), "v"(hi)); return r; }
; __device__ __forceinline__ void p0_prologue(Ctx& X) {
;     ...
;         for (int r = 0; r < 4; ++r)
; #pragma unroll
;             for (int j = 0; j < 8; ++j) s[r] += (v[r][j].x * v[r][j].x + v[r][j].y * v[r][j].y) + (v[r][j].z * v[r][j].z + v[r][j].w * v[r][j].w);
;         f32x4 w[8];
; #pragma unroll
;         for (int j = 0; j < 8; ++j) w[j] = wr_[64 * j];
; #pragma unroll
;         for (int r = 0; r < 4; ++r) { const int mm = m + r * NGW; if (mm >= T) break;
;             const float rstd = rsqrtf(wave_sum(s[r]) * (1.f / D) + EPS);
;             bf16* o8 = XP_U(X) + (size_t)(lane >> 4) * PANE_A + (size_t)mm * 64 + 4 * (lane & 15);
; #pragma unroll
;             for (int j = 0; j < 8; ++j) { u32x2 o; o.x = pk_bf16(v[r][j].x * rstd * w[j].x, v[r][j].y * rstd * w[j].y); o.y = pk_bf16(v[r][j].z * rstd * w[j].z, v[r][j].w * rstd * w[j].w); *(u32x2*)(o8 + (size_t)(4 * j) * PANE_A) = o; } }
	v_mov_b32_e32 v96, v155
	v_mov_b32_e32 v97, v151
	v_mov_b32_e32 v94, v154
	v_mov_b32_e32 v95, v150
	v_pk_mul_f32 v[96:97], v[96:97], v[96:97]
	v_mov_b32_e32 v98, v157
	v_mov_b32_e32 v99, v153
	v_pk_fma_f32 v[94:95], v[94:95], v[94:95], v[96:97]
	v_mov_b32_e32 v96, v156
	v_mov_b32_e32 v97, v152
	v_pk_mul_f32 v[98:99], v[98:99], v[98:99]
	s_nop 0
	v_pk_fma_f32 v[96:97], v[96:97], v[96:97], v[98:99]
	v_pk_mul_f32 v[98:99], v[146:147], v[146:147]
	v_pk_add_f32 v[94:95], v[94:95], v[96:97]
	v_pk_mul_f32 v[96:97], v[148:149], v[148:149]
	v_pk_add_f32 v[94:95], v[94:95], v[94:95] op_sel:[0,1] op_sel_hi:[1,0]
	v_pk_mov_b32 v[100:101], v[98:99], v[96:97] op_sel:[1,0]
	v_mov_b32_e32 v99, v97
	v_pk_add_f32 v[96:97], v[100:101], v[98:99]
	v_mul_f32_e32 v98, v134, v134
	v_mul_f32_e32 v99, v135, v135
	v_pk_add_f32 v[96:97], v[96:97], v[96:97] op_sel:[0,1] op_sel_hi:[1,0]
	v_mov_b32_e32 v95, v98
	v_mov_b32_e32 v97, v99
	v_pk_add_f32 v[94:95], v[94:95], v[96:97]
	v_mul_f32_e32 v96, v143, v143
	v_mul_f32_e32 v98, v145, v145
	v_mul_f32_e32 v100, v136, v136
	v_mul_f32_e32 v101, v137, v137
	v_pk_fma_f32 v[96:97], v[142:143], v[142:143], v[96:97] op_sel_hi:[1,1,0]
	v_pk_fma_f32 v[98:99], v[144:145], v[144:145], v[98:99] op_sel_hi:[1,1,0]
	v_mov_b32_e32 v97, v100
	v_mov_b32_e32 v99, v101
	v_pk_add_f32 v[96:97], v[96:97], v[98:99]
	v_pk_mul_f32 v[98:99], v[126:127], v[126:127]
	v_pk_add_f32 v[94:95], v[94:95], v[96:97]
	v_pk_mul_f32 v[96:97], v[128:129], v[128:129]
	v_pk_add_f32 v[94:95], v[94:95], v[94:95] op_sel:[0,1] op_sel_hi:[1,0]
	v_pk_mov_b32 v[100:101], v[98:99], v[96:97] op_sel:[1,0]
	v_mov_b32_e32 v99, v97
	v_pk_add_f32 v[96:97], v[100:101], v[98:99]
	v_mul_f32_e32 v98, v130, v130
	v_mul_f32_e32 v99, v131, v131
	v_pk_add_f32 v[96:97], v[96:97], v[96:97] op_sel:[0,1] op_sel_hi:[1,0]
	v_mov_b32_e32 v95, v98
	v_mov_b32_e32 v97, v99
	v_pk_add_f32 v[94:95], v[94:95], v[96:97]
	v_mul_f32_e32 v96, v139, v139
	v_mul_f32_e32 v98, v141, v141
	v_mul_f32_e32 v100, v132, v132
	v_mul_f32_e32 v101, v133, v133
	v_pk_fma_f32 v[96:97], v[138:139], v[138:139], v[96:97] op_sel_hi:[1,1,0]
	v_pk_fma_f32 v[98:99], v[140:141], v[140:141], v[98:99] op_sel_hi:[1,1,0]
	v_mov_b32_e32 v97, v100
	v_mov_b32_e32 v99, v101
	v_pk_add_f32 v[96:97], v[96:97], v[98:99]
	s_nop 0
	v_pk_add_f32 v[94:95], v[94:95], v[96:97]
	s_nop 0
	v_add_f32_e32 v94, v94, v95
	ds_bpermute_b32 v95, v182, v94
	s_waitcnt lgkmcnt(0)
	v_add_f32_e32 v94, v94, v95
	ds_bpermute_b32 v95, v183, v94
	s_waitcnt lgkmcnt(0)
	v_add_f32_e32 v94, v94, v95
	ds_bpermute_b32 v95, v184, v94
	s_waitcnt lgkmcnt(0)
	v_add_f32_e32 v94, v94, v95
	ds_bpermute_b32 v95, v185, v94
	s_waitcnt lgkmcnt(0)
	v_add_f32_e32 v94, v94, v95
	ds_bpermute_b32 v95, v186, v94
	s_waitcnt lgkmcnt(0)
	v_add_f32_e32 v94, v94, v95
	ds_bpermute_b32 v95, v187, v94
	s_waitcnt lgkmcnt(0)
	v_add_f32_e32 v94, v94, v95
	v_fmamk_f32 v94, v94, 0x3a000000, v188
	v_mul_f32_e32 v95, 0x4b800000, v94
	v_cmp_gt_f32_e32 vcc, s23, v94
	s_nop 1
	v_cndmask_b32_e32 v94, v94, v95, vcc
	v_rsq_f32_e32 v94, v94
	s_nop 0
	v_mul_f32_e32 v95, 0x45800000, v94
	v_cndmask_b32_e32 v100, v94, v95, vcc
	v_mul_f32_e32 v96, v154, v100
	v_mul_f32_e32 v97, v155, v100
	v_mul_f32_e32 v96, v2, v96
	v_mul_f32_e32 v97, v3, v97
	v_cvt_pk_bf16_f32 v96, v96, v97
	v_mul_f32_e32 v97, v156, v100
	v_mul_f32_e32 v98, v157, v100
	v_lshl_add_u64 v[94:95], v[178:179], 0, v[172:173]
	v_mul_f32_e32 v97, v4, v97
	v_mul_f32_e32 v98, v5, v98
	v_cvt_pk_bf16_f32 v97, v97, v98
	v_add_co_u32_e32 v98, vcc, s25, v94
	s_nop 1
	v_addc_co_u32_e32 v99, vcc, 0, v95, vcc
	global_store_dwordx2 v[98:99], v[96:97], off sc1
	v_mul_f32_e32 v96, v150, v100
	v_mul_f32_e32 v97, v151, v100
	v_mul_f32_e32 v96, v18, v96
	v_mul_f32_e32 v97, v19, v97
	v_cvt_pk_bf16_f32 v96, v96, v97
	v_mul_f32_e32 v97, v152, v100
	v_mul_f32_e32 v98, v153, v100
	v_mul_f32_e32 v97, v20, v97
	v_mul_f32_e32 v98, v21, v98
	v_cvt_pk_bf16_f32 v97, v97, v98
	v_add_co_u32_e32 v98, vcc, s26, v94
	s_nop 1
	v_addc_co_u32_e32 v99, vcc, 0, v95, vcc
	global_store_dwordx2 v[98:99], v[96:97], off sc1
	v_mul_f32_e32 v96, v146, v100
	v_mul_f32_e32 v97, v147, v100
	v_mul_f32_e32 v96, v14, v96
	v_mul_f32_e32 v97, v15, v97
	v_cvt_pk_bf16_f32 v96, v96, v97
	v_mul_f32_e32 v97, v148, v100
	v_mul_f32_e32 v98, v149, v100
	v_mul_f32_e32 v97, v16, v97
	v_mul_f32_e32 v98, v17, v98
	v_cvt_pk_bf16_f32 v97, v97, v98
	v_add_co_u32_e32 v98, vcc, s27, v94
	s_nop 1
	v_addc_co_u32_e32 v99, vcc, 0, v95, vcc
	global_store_dwordx2 v[98:99], v[96:97], off sc1
	v_mul_f32_e32 v96, v142, v100
	v_mul_f32_e32 v97, v143, v100
	v_mul_f32_e32 v96, v10, v96
	v_mul_f32_e32 v97, v11, v97
	v_cvt_pk_bf16_f32 v96, v96, v97
	v_mul_f32_e32 v97, v144, v100
	v_mul_f32_e32 v98, v145, v100
	v_mul_f32_e32 v97, v12, v97
	v_mul_f32_e32 v98, v13, v98
	v_cvt_pk_bf16_f32 v97, v97, v98
	v_add_co_u32_e32 v98, vcc, s28, v94
	s_nop 1
	v_addc_co_u32_e32 v99, vcc, 0, v95, vcc
	global_store_dwordx2 v[98:99], v[96:97], off sc1
	v_mul_f32_e32 v96, v134, v100
	v_mul_f32_e32 v97, v135, v100
	v_mul_f32_e32 v96, v6, v96
	v_mul_f32_e32 v97, v7, v97
	v_cvt_pk_bf16_f32 v96, v96, v97
	v_mul_f32_e32 v97, v136, v100
	v_mul_f32_e32 v98, v137, v100
	v_mul_f32_e32 v97, v8, v97
	v_mul_f32_e32 v98, v9, v98
	v_cvt_pk_bf16_f32 v97, v97, v98
	v_add_co_u32_e32 v98, vcc, s29, v94
	s_nop 1
	v_addc_co_u32_e32 v99, vcc, 0, v95, vcc
	global_store_dwordx2 v[98:99], v[96:97], off sc1
	v_mul_f32_e32 v96, v126, v100
	v_mul_f32_e32 v97, v127, v100
	v_mul_f32_e32 v96, v38, v96
	v_mul_f32_e32 v97, v39, v97
	v_cvt_pk_bf16_f32 v96, v96, v97
	v_mul_f32_e32 v97, v128, v100
	v_mul_f32_e32 v98, v129, v100
	v_mul_f32_e32 v97, v40, v97
	v_mul_f32_e32 v98, v41, v98
	v_cvt_pk_bf16_f32 v97, v97, v98
	v_add_co_u32_e32 v98, vcc, s30, v94
	s_nop 1
	v_addc_co_u32_e32 v99, vcc, 0, v95, vcc
	global_store_dwordx2 v[98:99], v[96:97], off sc1
	v_mul_f32_e32 v96, v138, v100
	v_mul_f32_e32 v97, v139, v100
	v_mul_f32_e32 v96, v34, v96
	v_mul_f32_e32 v97, v35, v97
	v_cvt_pk_bf16_f32 v96, v96, v97
	v_mul_f32_e32 v97, v140, v100
	v_mul_f32_e32 v98, v141, v100
	v_mul_f32_e32 v97, v36, v97
	v_mul_f32_e32 v98, v37, v98
	v_cvt_pk_bf16_f32 v97, v97, v98
	v_add_co_u32_e32 v98, vcc, s31, v94
	s_nop 1
	v_addc_co_u32_e32 v99, vcc, 0, v95, vcc
	global_store_dwordx2 v[98:99], v[96:97], off sc1
	v_mul_f32_e32 v96, v130, v100
	v_mul_f32_e32 v97, v131, v100
	v_mul_f32_e32 v96, v26, v96
	v_mul_f32_e32 v97, v27, v97
	v_add_co_u32_e32 v94, vcc, 0x5c00000, v94
	v_cvt_pk_bf16_f32 v96, v96, v97
	v_mul_f32_e32 v97, v132, v100
	s_nop 0
	v_addc_co_u32_e32 v95, vcc, 0, v95, vcc
	v_mul_f32_e32 v97, v28, v97
	v_mul_f32_e32 v98, v133, v100
	s_andn2_b64 vcc, exec, s[20:21]
	v_mul_f32_e32 v98, v29, v98
	v_cvt_pk_bf16_f32 v97, v97, v98
	global_store_dwordx2 v[94:95], v[96:97], off sc1
	s_cbranch_vccnz .LBB0_12
; __device__ __forceinline__ unsigned pk_bf16(float lo, float hi) { unsigned r; asm("v_cvt_pk_bf16_f32 %0, %1, %2" : "=v"(r) : "v"(lo), "v"(hi)); return r; }
; __device__ __forceinline__ void p0_prologue(Ctx& X) {
;     ...
;         for (int r = 0; r < 4; ++r)
; #pragma unroll
;             for (int j = 0; j < 8; ++j) s[r] += (v[r][j].x * v[r][j].x + v[r][j].y * v[r][j].y) + (v[r][j].z * v[r][j].z + v[r][j].w * v[r][j].w);
;         f32x4 w[8];
; #pragma unroll
;         for (int j = 0; j < 8; ++j) w[j] = wr_[64 * j];
; #pragma unroll
;         for (int r = 0; r < 4; ++r) { const int mm = m + r * NGW; if (mm >= T) break;
;             const float rstd = rsqrtf(wave_sum(s[r]) * (1.f / D) + EPS);
;             bf16* o8 = XP_U(X) + (size_t)(lane >> 4) * PANE_A + (size_t)mm * 64 + 4 * (lane & 15);
; #pragma unroll
;             for (int j = 0; j < 8; ++j) { u32x2 o; o.x = pk_bf16(v[r][j].x * rstd * w[j].x, v[r][j].y * rstd * w[j].y); o.y = pk_bf16(v[r][j].z * rstd * w[j].z, v[r][j].w * rstd * w[j].w); *(u32x2*)(o8 + (size_t)(4 * j) * PANE_A) = o; } }
	v_mul_f32_e32 v94, v103, v103
	v_mul_f32_e32 v95, v105, v105
	v_fmac_f32_e32 v94, v102, v102
	v_fmac_f32_e32 v95, v104, v104
	v_add_f32_e32 v94, v94, v95
	v_mul_f32_e32 v95, v91, v91
	v_mul_f32_e32 v96, v93, v93
	v_fmac_f32_e32 v95, v90, v90
	v_fmac_f32_e32 v96, v92, v92
	v_add_f32_e32 v95, v95, v96
	v_add_f32_e32 v94, v94, v95
	v_mul_f32_e32 v95, v87, v87
	v_mul_f32_e32 v96, v89, v89
	v_fmac_f32_e32 v95, v86, v86
	v_fmac_f32_e32 v96, v88, v88
	v_add_f32_e32 v95, v95, v96
	v_add_f32_e32 v94, v94, v95
	v_mul_f32_e32 v95, v83, v83
	v_mul_f32_e32 v96, v85, v85
	v_fmac_f32_e32 v95, v82, v82
	v_fmac_f32_e32 v96, v84, v84
	v_add_f32_e32 v95, v95, v96
	v_add_f32_e32 v94, v94, v95
	v_mul_f32_e32 v95, v79, v79
	v_mul_f32_e32 v96, v81, v81
	v_fmac_f32_e32 v95, v78, v78
	v_fmac_f32_e32 v96, v80, v80
	v_add_f32_e32 v95, v95, v96
	v_add_f32_e32 v94, v94, v95
	v_mul_f32_e32 v95, v75, v75
	v_mul_f32_e32 v96, v77, v77
	v_fmac_f32_e32 v95, v74, v74
	v_fmac_f32_e32 v96, v76, v76
	v_add_f32_e32 v95, v95, v96
	v_add_f32_e32 v94, v94, v95
	v_mul_f32_e32 v95, v71, v71
	v_mul_f32_e32 v96, v73, v73
	v_fmac_f32_e32 v95, v70, v70
	v_fmac_f32_e32 v96, v72, v72
	v_add_f32_e32 v95, v95, v96
	v_add_f32_e32 v94, v94, v95
	v_mul_f32_e32 v95, v67, v67
	v_mul_f32_e32 v96, v69, v69
	v_fmac_f32_e32 v95, v66, v66
	v_fmac_f32_e32 v96, v68, v68
	v_add_f32_e32 v95, v95, v96
	v_add_f32_e32 v94, v94, v95
	ds_bpermute_b32 v95, v182, v94
	s_ashr_i32 s19, s18, 31
	s_lshl_b64 s[2:3], s[18:19], 7
	s_waitcnt lgkmcnt(0)
	v_add_f32_e32 v94, v94, v95
	ds_bpermute_b32 v95, v183, v94
	s_waitcnt lgkmcnt(0)
	v_add_f32_e32 v94, v94, v95
	ds_bpermute_b32 v95, v184, v94
	s_waitcnt lgkmcnt(0)
	v_add_f32_e32 v94, v94, v95
	ds_bpermute_b32 v95, v185, v94
	s_waitcnt lgkmcnt(0)
	v_add_f32_e32 v94, v94, v95
	ds_bpermute_b32 v95, v186, v94
	s_waitcnt lgkmcnt(0)
	v_add_f32_e32 v94, v94, v95
	ds_bpermute_b32 v95, v187, v94
	s_waitcnt lgkmcnt(0)
	v_add_f32_e32 v94, v94, v95
	v_fmamk_f32 v94, v94, 0x3a000000, v188
	v_mul_f32_e32 v95, 0x4b800000, v94
	v_cmp_gt_f32_e32 vcc, s23, v94
	s_nop 1
	v_cndmask_b32_e32 v94, v94, v95, vcc
	v_rsq_f32_e32 v94, v94
	s_nop 0
	v_mul_f32_e32 v95, 0x45800000, v94
	v_cndmask_b32_e32 v98, v94, v95, vcc
	v_mul_f32_e32 v90, v90, v98
	v_mul_f32_e32 v91, v91, v98
	v_mul_f32_e32 v90, v18, v90
	v_mul_f32_e32 v91, v19, v91
	v_cvt_pk_bf16_f32 v90, v90, v91
	v_mul_f32_e32 v91, v92, v98
	v_mul_f32_e32 v92, v93, v98
	v_mul_f32_e32 v86, v86, v98
	v_mul_f32_e32 v87, v87, v98
	v_lshl_add_u64 v[94:95], v[170:171], 0, s[2:3]
	v_mul_f32_e32 v91, v20, v91
	v_mul_f32_e32 v92, v21, v92
	v_mul_f32_e32 v86, v14, v86
	v_mul_f32_e32 v87, v15, v87
	v_cvt_pk_bf16_f32 v91, v91, v92
	v_add_co_u32_e32 v92, vcc, s33, v94
	v_cvt_pk_bf16_f32 v86, v86, v87
	v_mul_f32_e32 v87, v88, v98
	v_mul_f32_e32 v88, v89, v98
	v_mul_f32_e32 v82, v82, v98
	v_mul_f32_e32 v83, v83, v98
	v_addc_co_u32_e32 v93, vcc, 0, v95, vcc
	v_mul_f32_e32 v87, v16, v87
	v_mul_f32_e32 v88, v17, v88
	v_mul_f32_e32 v82, v10, v82
	v_mul_f32_e32 v83, v11, v83
	v_cvt_pk_bf16_f32 v87, v87, v88
	v_add_co_u32_e32 v88, vcc, s23, v94
	v_cvt_pk_bf16_f32 v82, v82, v83
	v_mul_f32_e32 v83, v84, v98
	v_mul_f32_e32 v84, v85, v98
	v_mul_f32_e32 v78, v78, v98
	v_mul_f32_e32 v79, v79, v98
	v_addc_co_u32_e32 v89, vcc, 0, v95, vcc
	v_mul_f32_e32 v83, v12, v83
	v_mul_f32_e32 v84, v13, v84
	v_mul_f32_e32 v78, v6, v78
	v_mul_f32_e32 v79, v7, v79
	v_cvt_pk_bf16_f32 v83, v83, v84
	v_add_co_u32_e32 v84, vcc, s34, v94
	v_cvt_pk_bf16_f32 v78, v78, v79
	v_mul_f32_e32 v79, v80, v98
	v_mul_f32_e32 v80, v81, v98
	v_mul_f32_e32 v74, v74, v98
	v_mul_f32_e32 v75, v75, v98
	v_addc_co_u32_e32 v85, vcc, 0, v95, vcc
	v_mul_f32_e32 v79, v8, v79
	v_mul_f32_e32 v80, v9, v80
	v_mul_f32_e32 v74, v38, v74
	v_mul_f32_e32 v75, v39, v75
	v_cvt_pk_bf16_f32 v79, v79, v80
	v_add_co_u32_e32 v80, vcc, s35, v94
	v_cvt_pk_bf16_f32 v74, v74, v75
	v_mul_f32_e32 v75, v76, v98
	v_mul_f32_e32 v76, v77, v98
	v_mul_f32_e32 v70, v70, v98
	v_mul_f32_e32 v71, v71, v98
	v_addc_co_u32_e32 v81, vcc, 0, v95, vcc
	v_mul_f32_e32 v75, v40, v75
	v_mul_f32_e32 v76, v41, v76
	v_mul_f32_e32 v70, v34, v70
	v_mul_f32_e32 v71, v35, v71
	v_cvt_pk_bf16_f32 v75, v75, v76
	v_add_co_u32_e32 v76, vcc, s36, v94
	v_cvt_pk_bf16_f32 v70, v70, v71
	v_mul_f32_e32 v71, v72, v98
	v_mul_f32_e32 v72, v73, v98
	v_mul_f32_e32 v66, v66, v98
	v_mul_f32_e32 v67, v67, v98
	v_addc_co_u32_e32 v77, vcc, 0, v95, vcc
	v_mul_f32_e32 v71, v36, v71
	v_mul_f32_e32 v72, v37, v72
	v_mul_f32_e32 v66, v26, v66
	v_mul_f32_e32 v67, v27, v67
	v_cvt_pk_bf16_f32 v71, v71, v72
	v_add_co_u32_e32 v72, vcc, s37, v94
	v_cvt_pk_bf16_f32 v66, v66, v67
	v_mul_f32_e32 v67, v68, v98
	v_mul_f32_e32 v68, v69, v98
	v_mul_f32_e32 v96, v102, v98
	v_mul_f32_e32 v97, v103, v98
	v_addc_co_u32_e32 v73, vcc, 0, v95, vcc
	v_mul_f32_e32 v67, v28, v67
	v_mul_f32_e32 v68, v29, v68
	v_mul_f32_e32 v96, v2, v96
	v_mul_f32_e32 v97, v3, v97
	v_cvt_pk_bf16_f32 v67, v67, v68
	v_add_co_u32_e32 v68, vcc, 0x1c00000, v94
	v_cvt_pk_bf16_f32 v96, v96, v97
	v_mul_f32_e32 v97, v104, v98
	s_nop 0
	v_addc_co_u32_e32 v69, vcc, 0, v95, vcc
	v_mul_f32_e32 v97, v4, v97
	v_mul_f32_e32 v99, v105, v98
	s_andn2_b64 vcc, exec, s[16:17]
	v_mul_f32_e32 v99, v5, v99
	v_cvt_pk_bf16_f32 v97, v97, v99
	global_store_dwordx2 v[94:95], v[96:97], off sc1
	global_store_dwordx2 v[92:93], v[90:91], off sc1
	global_store_dwordx2 v[88:89], v[86:87], off sc1
	global_store_dwordx2 v[84:85], v[82:83], off sc1
	global_store_dwordx2 v[80:81], v[78:79], off sc1
	global_store_dwordx2 v[76:77], v[74:75], off sc1
	global_store_dwordx2 v[72:73], v[70:71], off sc1
	global_store_dwordx2 v[68:69], v[66:67], off sc1
	s_cbranch_vccnz .LBB0_12
; __device__ __forceinline__ unsigned pk_bf16(float lo, float hi) { unsigned r; asm("v_cvt_pk_bf16_f32 %0, %1, %2" : "=v"(r) : "v"(lo), "v"(hi)); return r; }
; __device__ __forceinline__ void p0_prologue(Ctx& X) {
;     ...
;         for (int r = 0; r < 4; ++r)
; #pragma unroll
;             for (int j = 0; j < 8; ++j) s[r] += (v[r][j].x * v[r][j].x + v[r][j].y * v[r][j].y) + (v[r][j].z * v[r][j].z + v[r][j].w * v[r][j].w);
;         f32x4 w[8];
; #pragma unroll
;         for (int j = 0; j < 8; ++j) w[j] = wr_[64 * j];
; #pragma unroll
;         for (int r = 0; r < 4; ++r) { const int mm = m + r * NGW; if (mm >= T) break;
;             const float rstd = rsqrtf(wave_sum(s[r]) * (1.f / D) + EPS);
;             bf16* o8 = XP_U(X) + (size_t)(lane >> 4) * PANE_A + (size_t)mm * 64 + 4 * (lane & 15);
; #pragma unroll
;             for (int j = 0; j < 8; ++j) { u32x2 o; o.x = pk_bf16(v[r][j].x * rstd * w[j].x, v[r][j].y * rstd * w[j].y); o.y = pk_bf16(v[r][j].z * rstd * w[j].z, v[r][j].w * rstd * w[j].w); *(u32x2*)(o8 + (size_t)(4 * j) * PANE_A) = o; } }
	v_mul_f32_e32 v66, v63, v63
	v_mul_f32_e32 v67, v65, v65
	v_fmac_f32_e32 v66, v62, v62
	v_fmac_f32_e32 v67, v64, v64
	v_add_f32_e32 v66, v66, v67
	v_mul_f32_e32 v67, v59, v59
	v_mul_f32_e32 v68, v61, v61
	v_fmac_f32_e32 v67, v58, v58
	v_fmac_f32_e32 v68, v60, v60
	v_add_f32_e32 v67, v67, v68
	v_add_f32_e32 v66, v66, v67
	v_mul_f32_e32 v67, v55, v55
	v_mul_f32_e32 v68, v57, v57
	v_fmac_f32_e32 v67, v54, v54
	v_fmac_f32_e32 v68, v56, v56
	v_add_f32_e32 v67, v67, v68
	v_add_f32_e32 v66, v66, v67
	v_mul_f32_e32 v67, v51, v51
	v_mul_f32_e32 v68, v53, v53
	v_fmac_f32_e32 v67, v50, v50
	v_fmac_f32_e32 v68, v52, v52
	v_add_f32_e32 v67, v67, v68
	v_add_f32_e32 v66, v66, v67
	v_mul_f32_e32 v67, v47, v47
	v_mul_f32_e32 v68, v49, v49
	v_fmac_f32_e32 v67, v46, v46
	v_fmac_f32_e32 v68, v48, v48
	v_add_f32_e32 v67, v67, v68
	v_add_f32_e32 v66, v66, v67
	v_mul_f32_e32 v67, v43, v43
	v_mul_f32_e32 v68, v45, v45
	v_fmac_f32_e32 v67, v42, v42
	v_fmac_f32_e32 v68, v44, v44
	v_add_f32_e32 v67, v67, v68
	v_add_f32_e32 v66, v66, v67
	v_mul_f32_e32 v67, v31, v31
	v_mul_f32_e32 v68, v33, v33
	v_fmac_f32_e32 v67, v30, v30
	v_fmac_f32_e32 v68, v32, v32
	v_add_f32_e32 v67, v67, v68
	v_add_f32_e32 v66, v66, v67
	v_mul_f32_e32 v67, v23, v23
	v_mul_f32_e32 v68, v25, v25
	v_fmac_f32_e32 v67, v22, v22
	v_fmac_f32_e32 v68, v24, v24
	v_add_f32_e32 v67, v67, v68
	v_add_f32_e32 v66, v66, v67
	ds_bpermute_b32 v67, v182, v66
	s_ashr_i32 s15, s14, 31
	s_lshl_b64 s[2:3], s[14:15], 7
	s_waitcnt lgkmcnt(0)
	v_add_f32_e32 v66, v66, v67
	ds_bpermute_b32 v67, v183, v66
	s_waitcnt lgkmcnt(0)
	v_add_f32_e32 v66, v66, v67
	ds_bpermute_b32 v67, v184, v66
	s_waitcnt lgkmcnt(0)
	v_add_f32_e32 v66, v66, v67
	ds_bpermute_b32 v67, v185, v66
	s_waitcnt lgkmcnt(0)
	v_add_f32_e32 v66, v66, v67
	ds_bpermute_b32 v67, v186, v66
	s_waitcnt lgkmcnt(0)
	v_add_f32_e32 v66, v66, v67
	ds_bpermute_b32 v67, v187, v66
	s_waitcnt lgkmcnt(0)
	v_add_f32_e32 v66, v66, v67
	v_fmamk_f32 v66, v66, 0x3a000000, v188
	v_mul_f32_e32 v67, 0x4b800000, v66
	v_cmp_gt_f32_e32 vcc, s23, v66
	s_nop 1
	v_cndmask_b32_e32 v66, v66, v67, vcc
	v_rsq_f32_e32 v66, v66
	s_nop 0
	v_mul_f32_e32 v67, 0x45800000, v66
	v_cndmask_b32_e32 v68, v66, v67, vcc
	v_mul_f32_e32 v62, v62, v68
	v_mul_f32_e32 v2, v2, v62
	v_mul_f32_e32 v62, v63, v68
	v_mul_f32_e32 v3, v3, v62
	v_cvt_pk_bf16_f32 v2, v2, v3
	v_mul_f32_e32 v3, v64, v68
	v_mul_f32_e32 v3, v4, v3
	v_mul_f32_e32 v4, v65, v68
	v_lshl_add_u64 v[66:67], v[170:171], 0, s[2:3]
	v_mul_f32_e32 v4, v5, v4
	v_cvt_pk_bf16_f32 v3, v3, v4
	global_store_dwordx2 v[66:67], v[2:3], off sc1
	v_mul_f32_e32 v2, v58, v68
	v_mul_f32_e32 v3, v59, v68
	v_mul_f32_e32 v2, v18, v2
	v_mul_f32_e32 v3, v19, v3
	v_cvt_pk_bf16_f32 v2, v2, v3
	v_mul_f32_e32 v3, v60, v68
	v_mul_f32_e32 v4, v61, v68
	v_mul_f32_e32 v3, v20, v3
	v_mul_f32_e32 v4, v21, v4
	v_cvt_pk_bf16_f32 v3, v3, v4
	v_add_co_u32_e32 v4, vcc, s33, v66
	s_nop 1
	v_addc_co_u32_e32 v5, vcc, 0, v67, vcc
	global_store_dwordx2 v[4:5], v[2:3], off sc1
	v_mul_f32_e32 v2, v54, v68
	v_mul_f32_e32 v3, v55, v68
	v_mul_f32_e32 v2, v14, v2
	v_mul_f32_e32 v3, v15, v3
	v_cvt_pk_bf16_f32 v2, v2, v3
	v_mul_f32_e32 v3, v56, v68
	v_mul_f32_e32 v4, v57, v68
	v_mul_f32_e32 v3, v16, v3
	v_mul_f32_e32 v4, v17, v4
	v_cvt_pk_bf16_f32 v3, v3, v4
	v_add_co_u32_e32 v4, vcc, s23, v66
	s_nop 1
	v_addc_co_u32_e32 v5, vcc, 0, v67, vcc
	global_store_dwordx2 v[4:5], v[2:3], off sc1
	v_mul_f32_e32 v2, v50, v68
	v_mul_f32_e32 v3, v51, v68
	v_mul_f32_e32 v2, v10, v2
	v_mul_f32_e32 v3, v11, v3
	v_cvt_pk_bf16_f32 v2, v2, v3
	v_mul_f32_e32 v3, v52, v68
	v_mul_f32_e32 v4, v53, v68
	v_mul_f32_e32 v3, v12, v3
	v_mul_f32_e32 v4, v13, v4
	v_cvt_pk_bf16_f32 v3, v3, v4
	v_add_co_u32_e32 v4, vcc, s34, v66
	s_nop 1
	v_addc_co_u32_e32 v5, vcc, 0, v67, vcc
	global_store_dwordx2 v[4:5], v[2:3], off sc1
	v_mul_f32_e32 v2, v46, v68
	v_mul_f32_e32 v3, v47, v68
	v_mul_f32_e32 v2, v6, v2
	v_mul_f32_e32 v3, v7, v3
	v_cvt_pk_bf16_f32 v2, v2, v3
	v_mul_f32_e32 v3, v48, v68
	v_mul_f32_e32 v4, v49, v68
	v_mul_f32_e32 v3, v8, v3
	v_mul_f32_e32 v4, v9, v4
	v_cvt_pk_bf16_f32 v3, v3, v4
	v_add_co_u32_e32 v4, vcc, s35, v66
	s_nop 1
	v_addc_co_u32_e32 v5, vcc, 0, v67, vcc
	global_store_dwordx2 v[4:5], v[2:3], off sc1
	v_mul_f32_e32 v2, v42, v68
	v_mul_f32_e32 v3, v43, v68
	v_mul_f32_e32 v2, v38, v2
	v_mul_f32_e32 v3, v39, v3
	v_cvt_pk_bf16_f32 v2, v2, v3
	v_mul_f32_e32 v3, v44, v68
	v_mul_f32_e32 v4, v45, v68
	v_mul_f32_e32 v3, v40, v3
	v_mul_f32_e32 v4, v41, v4
	v_cvt_pk_bf16_f32 v3, v3, v4
	v_add_co_u32_e32 v4, vcc, s36, v66
	s_nop 1
	v_addc_co_u32_e32 v5, vcc, 0, v67, vcc
	global_store_dwordx2 v[4:5], v[2:3], off sc1
	v_mul_f32_e32 v2, v30, v68
	v_mul_f32_e32 v3, v31, v68
	v_mul_f32_e32 v2, v34, v2
	v_mul_f32_e32 v3, v35, v3
	v_cvt_pk_bf16_f32 v2, v2, v3
	v_mul_f32_e32 v3, v32, v68
	v_mul_f32_e32 v4, v33, v68
	v_mul_f32_e32 v3, v36, v3
	v_mul_f32_e32 v4, v37, v4
	v_cvt_pk_bf16_f32 v3, v3, v4
	v_add_co_u32_e32 v4, vcc, s37, v66
	s_nop 1
	v_addc_co_u32_e32 v5, vcc, 0, v67, vcc
	global_store_dwordx2 v[4:5], v[2:3], off sc1
	v_mul_f32_e32 v2, v22, v68
	v_mul_f32_e32 v3, v23, v68
	v_mul_f32_e32 v2, v26, v2
	v_mul_f32_e32 v3, v27, v3
	v_cvt_pk_bf16_f32 v2, v2, v3
	v_mul_f32_e32 v3, v24, v68
	v_mul_f32_e32 v4, v25, v68
	v_mul_f32_e32 v3, v28, v3
	v_mul_f32_e32 v4, v29, v4
	v_cvt_pk_bf16_f32 v3, v3, v4
	v_add_co_u32_e32 v4, vcc, 0x1c00000, v66
	s_nop 1
	v_addc_co_u32_e32 v5, vcc, 0, v67, vcc
	global_store_dwordx2 v[4:5], v[2:3], off sc1
	s_branch .LBB0_12

; __device__ __forceinline__ void p0_prologue(Ctx& X) {
;     ...
;     { constexpr int per = (LDP - NPROJ) * 64 * 2 / 16; const u32x4 z = {0u, 0u, 0u, 0u};
;       for (int i = gt; i < 32 * per; i += NGT) { const int kb = i / per, r = i - kb * per; ((u32x4*)(XP_WinT(X) + (size_t)kb * PANE_WIN + (size_t)NPROJ * 64))[r] = z; } }
.LBB0_22:
	v_mul_hi_i32 v9, v8, s3
	v_add_u32_e32 v9, v9, v8
	v_lshrrev_b32_e32 v10, 31, v9
	v_ashrrev_i32_e32 v9, 10, v9
	v_add_u32_e32 v9, v9, v10
	v_mad_i32_i24 v10, v9, s11, v8
	v_mul_hi_i32_i24_e32 v13, 0xd8000, v9
	v_mul_i32_i24_e32 v12, 0xd8000, v9
	v_add_u32_e32 v8, s2, v8
	v_lshl_add_u64 v[12:13], s[90:91], 0, v[12:13]
	v_ashrrev_i32_e32 v11, 31, v10
	v_cmp_lt_i32_e32 vcc, s12, v8
	v_lshl_add_u64 v[10:11], v[10:11], 4, v[12:13]
	s_or_b64 s[6:7], vcc, s[6:7]
	v_add_co_u32_e32 v10, vcc, 0x2d0000, v10
	s_nop 1
	v_addc_co_u32_e32 v11, vcc, 0, v11, vcc
	global_store_dwordx4 v[10:11], v[2:5], off offset:2048 sc1
	s_andn2_b64 exec, exec, s[6:7]
	s_cbranch_execnz .LBB0_22

; __device__ __forceinline__ unsigned pk_bf16(float lo, float hi) { unsigned r; asm("v_cvt_pk_bf16_f32 %0, %1, %2" : "=v"(r) : "v"(lo), "v"(hi)); return r; }
; __device__ __forceinline__ void tr_store(bf16* WT, int N, int pan, int kb, int nb, int lane, const f32x4 (&v)[8]) {
;     const int k0 = kb * 64 + 8 * (lane & 7), n0 = nb * 32 + 4 * (lane >> 3);
;     if (n0 < N) {
; #pragma unroll
;         for (int j = 0; j < 4; ++j) { u32x4 o; o.x = pk_bf16(v[0][j], v[1][j]); o.y = pk_bf16(v[2][j], v[3][j]); o.z = pk_bf16(v[4][j], v[5][j]); o.w = pk_bf16(v[6][j], v[7][j]);
;             *(u32x4*)(WT + (size_t)kb * pan + (size_t)(n0 + j) * 64 + 8 * (lane & 7)) = o; }
;     }
.LBB0_47:
	s_add_u32 s18, s90, s18
	s_mul_hi_i32 s3, s16, s25
	s_mul_i32 s2, s16, s25
	s_addc_u32 s19, s91, s19
	s_lshl_b64 s[2:3], s[2:3], 1
	s_add_u32 s2, s18, s2
	s_addc_u32 s3, s19, s3
	v_lshlrev_b32_e32 v68, 1, v66
	v_lshl_add_u64 v[78:79], s[2:3], 0, v[68:69]
	v_lshlrev_b64 v[80:81], 7, v[70:71]
	v_lshl_add_u64 v[80:81], v[78:79], 0, v[80:81]
	s_waitcnt vmcnt(6)
	v_cvt_pk_bf16_f32 v74, v10, v14
	s_waitcnt vmcnt(4)
	v_cvt_pk_bf16_f32 v75, v26, v34
	s_waitcnt vmcnt(2)
	v_cvt_pk_bf16_f32 v76, v46, v54
	s_waitcnt vmcnt(0)
	v_cvt_pk_bf16_f32 v77, v58, v62
	global_store_dwordx4 v[80:81], v[74:77], off sc1
	v_or_b32_e32 v80, 1, v70
	v_ashrrev_i32_e32 v81, 31, v80
	v_lshlrev_b64 v[80:81], 7, v[80:81]
	v_lshl_add_u64 v[80:81], v[78:79], 0, v[80:81]
	v_cvt_pk_bf16_f32 v74, v11, v15
	v_cvt_pk_bf16_f32 v75, v27, v35
	v_cvt_pk_bf16_f32 v76, v47, v55
	v_cvt_pk_bf16_f32 v77, v59, v63
	global_store_dwordx4 v[80:81], v[74:77], off sc1
	v_or_b32_e32 v80, 2, v70
	v_or_b32_e32 v70, 3, v70
	v_ashrrev_i32_e32 v81, 31, v80
	v_ashrrev_i32_e32 v71, 31, v70
	v_lshlrev_b64 v[80:81], 7, v[80:81]
	v_lshlrev_b64 v[70:71], 7, v[70:71]
	v_cvt_pk_bf16_f32 v74, v12, v16
	v_cvt_pk_bf16_f32 v75, v28, v36
	v_cvt_pk_bf16_f32 v76, v48, v56
	v_cvt_pk_bf16_f32 v77, v60, v64
	v_lshl_add_u64 v[80:81], v[78:79], 0, v[80:81]
	v_lshl_add_u64 v[70:71], v[78:79], 0, v[70:71]
	global_store_dwordx4 v[80:81], v[74:77], off sc1
	s_nop 1
	v_cvt_pk_bf16_f32 v74, v13, v17
	v_cvt_pk_bf16_f32 v75, v29, v37
	v_cvt_pk_bf16_f32 v76, v49, v57
	v_cvt_pk_bf16_f32 v77, v61, v65
	global_store_dwordx4 v[70:71], v[74:77], off sc1
	s_or_b64 exec, exec, s[6:7]
	s_and_b64 vcc, exec, s[4:5]
	s_cbranch_vccnz .LBB0_29
.LBB0_48:
	v_cmp_gt_i32_e32 vcc, s13, v72
	s_and_saveexec_b64 s[2:3], vcc
	s_cbranch_execz .LBB0_28
	s_mul_hi_i32 s5, s12, s17
	s_mul_i32 s4, s12, s17
	s_lshl_b64 s[4:5], s[4:5], 1
	s_add_u32 s4, s14, s4
	s_addc_u32 s5, s15, s5
	v_lshlrev_b32_e32 v68, 1, v66
	v_ashrrev_i32_e32 v73, 31, v72
	v_lshl_add_u64 v[70:71], s[4:5], 0, v[68:69]
	v_lshlrev_b64 v[78:79], 7, v[72:73]
	v_lshl_add_u64 v[78:79], v[70:71], 0, v[78:79]
	s_waitcnt vmcnt(6)
	v_cvt_pk_bf16_f32 v74, v2, v6
	s_waitcnt vmcnt(4)
	v_cvt_pk_bf16_f32 v75, v18, v22
	s_waitcnt vmcnt(2)
	v_cvt_pk_bf16_f32 v76, v30, v38
	s_waitcnt vmcnt(0)
	v_cvt_pk_bf16_f32 v77, v42, v50
	global_store_dwordx4 v[78:79], v[74:77], off sc1
	v_or_b32_e32 v78, 1, v72
	v_ashrrev_i32_e32 v79, 31, v78
	v_lshlrev_b64 v[78:79], 7, v[78:79]
	v_lshl_add_u64 v[78:79], v[70:71], 0, v[78:79]
	v_cvt_pk_bf16_f32 v74, v3, v7
	v_cvt_pk_bf16_f32 v75, v19, v23
	v_cvt_pk_bf16_f32 v76, v31, v39
	v_cvt_pk_bf16_f32 v77, v43, v51
	global_store_dwordx4 v[78:79], v[74:77], off sc1
	v_or_b32_e32 v78, 2, v72
	v_or_b32_e32 v72, 3, v72
	v_ashrrev_i32_e32 v79, 31, v78
	v_ashrrev_i32_e32 v73, 31, v72
	v_lshlrev_b64 v[78:79], 7, v[78:79]
	v_lshlrev_b64 v[72:73], 7, v[72:73]
	v_cvt_pk_bf16_f32 v74, v4, v8
	v_cvt_pk_bf16_f32 v75, v20, v24
	v_cvt_pk_bf16_f32 v76, v32, v40
	v_cvt_pk_bf16_f32 v77, v44, v52
	v_lshl_add_u64 v[78:79], v[70:71], 0, v[78:79]
	v_lshl_add_u64 v[70:71], v[70:71], 0, v[72:73]
	global_store_dwordx4 v[78:79], v[74:77], off sc1
	s_nop 1
	v_cvt_pk_bf16_f32 v74, v5, v9
	v_cvt_pk_bf16_f32 v75, v21, v25
	v_cvt_pk_bf16_f32 v76, v33, v41
	v_cvt_pk_bf16_f32 v77, v45, v53
	global_store_dwordx4 v[70:71], v[74:77], off sc1
	s_branch .LBB0_28

; __device__ __forceinline__ unsigned pk_bf16(float lo, float hi) { unsigned r; asm("v_cvt_pk_bf16_f32 %0, %1, %2" : "=v"(r) : "v"(lo), "v"(hi)); return r; }
;     __device__ __forceinline__ void operator()(const f32x4 (&acc)[2][2][4][2], const pg8::Unit& u, int wr, int wc, int fr_, int fq_, const LAS uchar* bl) const {
;     ...
; #pragma unroll
;             for (int ai = 0; ai < 2; ++ai)
; #pragma unroll
;                 for (int m = 0; m < 4; ++m) { bf16* rowp = O + (size_t)(u.col0 >> 8) * PANP + (size_t)(row0 + ai * 128 + m * 16) * 256 + (col0 & 255);
; #pragma unroll
;                     for (int bj = 0; bj < 2; ++bj) { const f32x4 v0 = acc[ai][bj][m][0], v1 = acc[ai][bj][m][1];
;                         u32x4 w; w.x = pk_bf16(v0[0], v0[1]); w.y = pk_bf16(v0[2], v0[3]); w.z = pk_bf16(v1[0], v1[1]); w.w = pk_bf16(v1[2], v1[3]);
;                         *(u32x4*)(rowp + bj * 128) = w; } }
.LBB0_116:
	s_andn2_b64 vcc, exec, s[2:3]
	s_mov_b64 s[2:3], -1
	global_store_dwordx4 v[136:137], v[130:133], off offset:256 sc1
	s_cbranch_vccnz .LBB0_107
	s_branch .LBB0_119
.LBB0_117:
	s_lshr_b32 s8, s79, 8
	s_lshl_b64 s[38:39], s[8:9], 22
	s_add_u32 s38, s67, s38
	s_addc_u32 s39, s68, s39
	v_lshlrev_b64 v[130:131], 9, v[134:135]
	v_lshl_add_u64 v[130:131], s[38:39], 0, v[130:131]
	v_lshl_add_u64 v[130:131], v[130:131], 0, v[190:191]
	s_movk_i32 s8, 0x2000
	v_cvt_pk_bf16_f32 v140, v126, v127
	v_cvt_pk_bf16_f32 v141, v128, v129
	v_cvt_pk_bf16_f32 v142, v122, v123
	v_cvt_pk_bf16_f32 v143, v124, v125
	v_add_co_u32_e32 v136, vcc, s8, v130
	global_store_dwordx4 v[130:131], v[140:143], off sc1
	s_nop 0
	v_addc_co_u32_e32 v137, vcc, 0, v131, vcc
	v_cvt_pk_bf16_f32 v140, v118, v119
	v_cvt_pk_bf16_f32 v141, v120, v121
	v_cvt_pk_bf16_f32 v142, v114, v115
	v_cvt_pk_bf16_f32 v143, v116, v117
	global_store_dwordx4 v[130:131], v[140:143], off offset:256 sc1
	v_lshl_add_u64 v[132:133], v[130:131], 0, s[20:21]
	s_nop 0
	v_cvt_pk_bf16_f32 v140, v110, v111
	v_cvt_pk_bf16_f32 v141, v112, v113
	v_cvt_pk_bf16_f32 v142, v106, v107
	v_cvt_pk_bf16_f32 v143, v108, v109
	global_store_dwordx4 v[136:137], v[140:143], off sc1
	v_add_co_u32_e32 v136, vcc, s61, v130
	s_nop 0
	v_cvt_pk_bf16_f32 v140, v102, v103
	v_cvt_pk_bf16_f32 v141, v104, v105
	v_cvt_pk_bf16_f32 v142, v98, v99
	v_cvt_pk_bf16_f32 v143, v100, v101
	s_nop 0
	v_addc_co_u32_e32 v137, vcc, 0, v131, vcc
	global_store_dwordx4 v[132:133], v[140:143], off offset:256 sc1
	v_lshl_add_u64 v[132:133], v[130:131], 0, s[10:11]
	s_nop 0
	v_cvt_pk_bf16_f32 v140, v94, v95
	v_cvt_pk_bf16_f32 v141, v96, v97
	v_cvt_pk_bf16_f32 v142, v90, v91
	v_cvt_pk_bf16_f32 v143, v92, v93
	global_store_dwordx4 v[136:137], v[140:143], off sc1
	v_add_co_u32_e32 v136, vcc, s66, v130
	s_nop 0
	v_cvt_pk_bf16_f32 v140, v86, v87
	v_cvt_pk_bf16_f32 v141, v88, v89
	v_cvt_pk_bf16_f32 v142, v82, v83
	v_cvt_pk_bf16_f32 v143, v84, v85
	s_nop 0
	v_addc_co_u32_e32 v137, vcc, 0, v131, vcc
	global_store_dwordx4 v[132:133], v[140:143], off offset:256 sc1
	v_lshl_add_u64 v[132:133], v[130:131], 0, s[22:23]
	s_nop 0
	v_cvt_pk_bf16_f32 v140, v78, v79
	v_cvt_pk_bf16_f32 v141, v80, v81
	v_cvt_pk_bf16_f32 v142, v74, v75
	v_cvt_pk_bf16_f32 v143, v76, v77
	global_store_dwordx4 v[136:137], v[140:143], off sc1
	v_add_co_u32_e32 v136, vcc, s62, v130
	s_nop 0
	v_cvt_pk_bf16_f32 v140, v70, v71
	v_cvt_pk_bf16_f32 v141, v72, v73
	v_cvt_pk_bf16_f32 v142, v66, v67
	v_cvt_pk_bf16_f32 v143, v68, v69
	s_nop 0
	v_addc_co_u32_e32 v137, vcc, 0, v131, vcc
	global_store_dwordx4 v[132:133], v[140:143], off offset:256 sc1
	v_lshl_add_u64 v[132:133], v[130:131], 0, s[24:25]
	s_nop 0
	v_cvt_pk_bf16_f32 v140, v62, v63
	v_cvt_pk_bf16_f32 v141, v64, v65
	v_cvt_pk_bf16_f32 v142, v58, v59
	v_cvt_pk_bf16_f32 v143, v60, v61
	global_store_dwordx4 v[136:137], v[140:143], off sc1
	v_add_co_u32_e32 v136, vcc, s63, v130
	s_nop 0
	v_cvt_pk_bf16_f32 v140, v54, v55
	v_cvt_pk_bf16_f32 v141, v56, v57
	v_cvt_pk_bf16_f32 v142, v50, v51
	v_cvt_pk_bf16_f32 v143, v52, v53
	s_nop 0
	v_addc_co_u32_e32 v137, vcc, 0, v131, vcc
	global_store_dwordx4 v[132:133], v[140:143], off offset:256 sc1
	v_lshl_add_u64 v[132:133], v[130:131], 0, s[26:27]
	s_nop 0
	v_cvt_pk_bf16_f32 v140, v46, v47
	v_cvt_pk_bf16_f32 v141, v48, v49
	v_cvt_pk_bf16_f32 v142, v42, v43
	v_cvt_pk_bf16_f32 v143, v44, v45
	global_store_dwordx4 v[136:137], v[140:143], off sc1
	v_add_co_u32_e32 v136, vcc, s64, v130
	s_nop 0
	v_cvt_pk_bf16_f32 v140, v38, v39
	v_cvt_pk_bf16_f32 v141, v40, v41
	v_cvt_pk_bf16_f32 v142, v34, v35
	v_cvt_pk_bf16_f32 v143, v36, v37
	s_nop 0
	v_addc_co_u32_e32 v137, vcc, 0, v131, vcc
	global_store_dwordx4 v[132:133], v[140:143], off offset:256 sc1
	v_lshl_add_u64 v[132:133], v[130:131], 0, s[28:29]
	s_nop 0
	v_cvt_pk_bf16_f32 v140, v30, v31
	v_cvt_pk_bf16_f32 v141, v32, v33
	v_cvt_pk_bf16_f32 v142, v26, v27
	v_cvt_pk_bf16_f32 v143, v28, v29
	global_store_dwordx4 v[136:137], v[140:143], off sc1
	v_lshl_add_u64 v[136:137], v[130:131], 0, s[30:31]
	v_add_co_u32_e32 v130, vcc, s65, v130
	v_cvt_pk_bf16_f32 v140, v22, v23
	v_cvt_pk_bf16_f32 v141, v24, v25
	v_cvt_pk_bf16_f32 v142, v18, v19
	v_cvt_pk_bf16_f32 v143, v20, v21
	s_nop 1
	v_addc_co_u32_e32 v131, vcc, 0, v131, vcc
	global_store_dwordx4 v[132:133], v[140:143], off offset:256 sc1
	v_cvt_pk_bf16_f32 v132, v2, v3
	v_cvt_pk_bf16_f32 v133, v4, v5
	s_nop 1
	v_cvt_pk_bf16_f32 v140, v14, v15
	v_cvt_pk_bf16_f32 v141, v16, v17
	v_cvt_pk_bf16_f32 v142, v10, v11
	v_cvt_pk_bf16_f32 v143, v12, v13
	global_store_dwordx4 v[130:131], v[140:143], off sc1
	v_cvt_pk_bf16_f32 v130, v6, v7
	v_cvt_pk_bf16_f32 v131, v8, v9
	s_cbranch_execnz .LBB0_116
; __device__ __forceinline__ unsigned pk_bf16(float lo, float hi) { unsigned r; asm("v_cvt_pk_bf16_f32 %0, %1, %2" : "=v"(r) : "v"(lo), "v"(hi)); return r; }
;     __device__ __forceinline__ void operator()(const f32x4 (&acc)[2][2][4][2], const pg8::Unit& u, int wr, int wc, int fr_, int fq_, const LAS uchar* bl) const {
;     ...
;         if (u.col0 < 2048) {
;             const float sc = (u.col0 >= 1024) ? 0.0625f : 1.0f; const int i0 = wc * 32 + 8 * fq;
; #pragma unroll
;             for (int ai = 0; ai < 2; ++ai) {
;                 f32x4 cs[4][4];
; #pragma unroll
;                 for (int m = 0; m < 4; ++m) { const int t = row0 + ai * 128 + m * 16;
;                     cs[m][0] = *(const f32x4*)(COS + (size_t)t * 128 + i0); cs[m][1] = *(const f32x4*)(COS + (size_t)t * 128 + i0 + 4); cs[m][2] = *(const f32x4*)(SIN + (size_t)t * 128 + i0); cs[m][3] = *(const f32x4*)(SIN + (size_t)t * 128 + i0 + 4); }
; #pragma unroll
;                 for (int m = 0; m < 4; ++m) { const int t = row0 + ai * 128 + m * 16; bf16* rowp = O + (size_t)(u.col0 >> 8) * PANP + (size_t)t * 256 + (col0 & 255);
;                     const f32x4 c0 = cs[m][0], c1 = cs[m][1], s0 = cs[m][2], s1 = cs[m][3];
;                     const f32x4 a0 = acc[ai][0][m][0], a1 = acc[ai][0][m][1], b0 = acc[ai][1][m][0], b1 = acc[ai][1][m][1];
;                     const f32x4 p0 = (a0 * c0 - b0 * s0) * sc, p1 = (a1 * c1 - b1 * s1) * sc, q0 = (b0 * c0 + a0 * s0) * sc, q1 = (b1 * c1 + a1 * s1) * sc;
;                     u32x4 w; w.x = pk_bf16(p0[0], p0[1]); w.y = pk_bf16(p0[2], p0[3]); w.z = pk_bf16(p1[0], p1[1]); w.w = pk_bf16(p1[2], p1[3]); *(u32x4*)rowp = w;
;                     w.x = pk_bf16(q0[0], q0[1]); w.y = pk_bf16(q0[2], q0[3]); w.z = pk_bf16(q1[0], q1[1]); w.w = pk_bf16(q1[2], q1[3]); *(u32x4*)(rowp + 128) = w; } }
.LBB0_118:
	v_or_b32_e32 v130, s70, v138
	v_lshlrev_b32_e32 v130, 2, v130
	v_mov_b32_e32 v131, v191
	v_lshl_add_u64 v[204:205], s[14:15], 0, v[130:131]
	v_lshlrev_b64 v[208:209], 9, v[134:135]
	v_lshl_add_u64 v[206:207], s[16:17], 0, v[130:131]
	v_lshl_add_u64 v[130:131], v[204:205], 0, v[208:209]
	global_load_dwordx4 v[222:225], v[130:131], off offset:16
	global_load_dwordx4 v[226:229], v[130:131], off
	v_lshl_add_u64 v[130:131], v[206:207], 0, v[208:209]
	global_load_dwordx4 v[230:233], v[130:131], off offset:16
	global_load_dwordx4 v[234:237], v[130:131], off
	v_lshl_add_u64 v[214:215], v[208:209], 0, s[20:21]
	v_lshl_add_u64 v[130:131], v[204:205], 0, v[214:215]
	global_load_dwordx4 v[146:149], v[130:131], off offset:16
	global_load_dwordx4 v[162:165], v[130:131], off
	v_lshl_add_u64 v[130:131], v[206:207], 0, v[214:215]
	global_load_dwordx4 v[170:173], v[130:131], off offset:16
	global_load_dwordx4 v[174:177], v[130:131], off
	v_lshl_add_u64 v[212:213], v[208:209], 0, s[10:11]
	v_lshl_add_u64 v[130:131], v[204:205], 0, v[212:213]
	global_load_dwordx4 v[138:141], v[130:131], off offset:16
	global_load_dwordx4 v[150:153], v[130:131], off
	v_lshl_add_u64 v[130:131], v[206:207], 0, v[212:213]
	global_load_dwordx4 v[142:145], v[130:131], off offset:16
	global_load_dwordx4 v[158:161], v[130:131], off
	v_lshl_add_u64 v[210:211], v[208:209], 0, s[22:23]
	v_lshl_add_u64 v[134:135], v[204:205], 0, v[210:211]
	v_lshl_add_u64 v[166:167], v[206:207], 0, v[210:211]
	global_load_dwordx4 v[130:133], v[134:135], off offset:16
	s_nop 0
	global_load_dwordx4 v[134:137], v[134:135], off
	s_nop 0
	global_load_dwordx4 v[154:157], v[166:167], off offset:16
	s_nop 0
	global_load_dwordx4 v[166:169], v[166:167], off
	s_cmpk_gt_i32 s79, 0x3ff
	s_cselect_b64 vcc, -1, 0
	s_ashr_i32 s38, s79, 8
	s_ashr_i32 s39, s38, 31
	s_lshl_b64 s[38:39], s[38:39], 22
	s_add_u32 s38, s67, s38
	s_addc_u32 s39, s68, s39
	v_cndmask_b32_e32 v202, 1.0, v220, vcc
	v_lshl_add_u64 v[238:239], s[38:39], 0, v[208:209]
	v_lshl_add_u64 v[238:239], v[238:239], 0, v[190:191]
	s_waitcnt vmcnt(0)
	v_pk_mul_f32 v[244:245], v[116:117], v[232:233]
	v_pk_mul_f32 v[240:241], v[120:121], v[236:237]
	v_pk_mul_f32 v[246:247], v[114:115], v[230:231]
	v_pk_fma_f32 v[244:245], v[124:125], v[224:225], v[244:245] neg_lo:[0,0,1] neg_hi:[0,0,1]
	v_pk_mul_f32 v[124:125], v[124:125], v[232:233]
	v_pk_mul_f32 v[242:243], v[118:119], v[234:235]
	v_pk_fma_f32 v[240:241], v[128:129], v[228:229], v[240:241] neg_lo:[0,0,1] neg_hi:[0,0,1]
	v_pk_fma_f32 v[246:247], v[122:123], v[222:223], v[246:247] neg_lo:[0,0,1] neg_hi:[0,0,1]
	v_pk_mul_f32 v[128:129], v[128:129], v[236:237]
	v_pk_mul_f32 v[122:123], v[122:123], v[230:231]
	v_pk_fma_f32 v[116:117], v[116:117], v[224:225], v[124:125]
	v_pk_fma_f32 v[242:243], v[126:127], v[226:227], v[242:243] neg_lo:[0,0,1] neg_hi:[0,0,1]
	v_pk_mul_f32 v[244:245], v[202:203], v[244:245] op_sel_hi:[0,1]
	v_pk_mul_f32 v[246:247], v[202:203], v[246:247] op_sel_hi:[0,1]
	v_pk_mul_f32 v[126:127], v[126:127], v[234:235]
	v_pk_fma_f32 v[120:121], v[120:121], v[228:229], v[128:129]
	v_pk_fma_f32 v[114:115], v[114:115], v[222:223], v[122:123]
	v_pk_mul_f32 v[122:123], v[202:203], v[116:117] op_sel_hi:[0,1]
	v_cvt_pk_bf16_f32 v116, v246, v247
	v_cvt_pk_bf16_f32 v117, v244, v245
	v_pk_mul_f32 v[240:241], v[202:203], v[240:241] op_sel_hi:[0,1]
	v_pk_mul_f32 v[242:243], v[202:203], v[242:243] op_sel_hi:[0,1]
	v_pk_fma_f32 v[118:119], v[118:119], v[226:227], v[126:127]
	v_pk_mul_f32 v[120:121], v[202:203], v[120:121] op_sel_hi:[0,1]
	v_pk_mul_f32 v[124:125], v[202:203], v[114:115] op_sel_hi:[0,1]
	v_cvt_pk_bf16_f32 v114, v242, v243
	v_cvt_pk_bf16_f32 v115, v240, v241
	global_store_dwordx4 v[238:239], v[114:117], off sc1
	v_pk_mul_f32 v[118:119], v[202:203], v[118:119] op_sel_hi:[0,1]
	s_nop 0
	v_cvt_pk_bf16_f32 v116, v124, v125
	v_cvt_pk_bf16_f32 v117, v122, v123
	v_cvt_pk_bf16_f32 v114, v118, v119
	v_cvt_pk_bf16_f32 v115, v120, v121
	global_store_dwordx4 v[238:239], v[114:117], off offset:256 sc1
	v_pk_mul_f32 v[120:121], v[100:101], v[172:173]
	v_pk_mul_f32 v[122:123], v[98:99], v[170:171]
	v_pk_mul_f32 v[116:117], v[104:105], v[176:177]
	v_pk_mul_f32 v[118:119], v[102:103], v[174:175]
	v_pk_fma_f32 v[116:117], v[112:113], v[164:165], v[116:117] neg_lo:[0,0,1] neg_hi:[0,0,1]
	v_pk_fma_f32 v[120:121], v[108:109], v[148:149], v[120:121] neg_lo:[0,0,1] neg_hi:[0,0,1]
	v_pk_fma_f32 v[122:123], v[106:107], v[146:147], v[122:123] neg_lo:[0,0,1] neg_hi:[0,0,1]
	v_pk_mul_f32 v[112:113], v[112:113], v[176:177]
	v_pk_mul_f32 v[108:109], v[108:109], v[172:173]
	v_pk_mul_f32 v[106:107], v[106:107], v[170:171]
	v_lshl_add_u64 v[114:115], s[38:39], 0, v[214:215]
	v_pk_fma_f32 v[118:119], v[110:111], v[162:163], v[118:119] neg_lo:[0,0,1] neg_hi:[0,0,1]
	v_pk_mul_f32 v[110:111], v[110:111], v[174:175]
	v_pk_fma_f32 v[104:105], v[104:105], v[164:165], v[112:113]
	v_pk_fma_f32 v[100:101], v[100:101], v[148:149], v[108:109]
	v_pk_fma_f32 v[98:99], v[98:99], v[146:147], v[106:107]
	v_lshl_add_u64 v[114:115], v[114:115], 0, v[190:191]
	v_pk_mul_f32 v[116:117], v[202:203], v[116:117] op_sel_hi:[0,1]
	v_pk_mul_f32 v[120:121], v[202:203], v[120:121] op_sel_hi:[0,1]
	v_pk_mul_f32 v[122:123], v[202:203], v[122:123] op_sel_hi:[0,1]
	v_pk_fma_f32 v[102:103], v[102:103], v[162:163], v[110:111]
	v_pk_mul_f32 v[104:105], v[202:203], v[104:105] op_sel_hi:[0,1]
	v_pk_mul_f32 v[106:107], v[202:203], v[100:101] op_sel_hi:[0,1]
	v_pk_mul_f32 v[108:109], v[202:203], v[98:99] op_sel_hi:[0,1]
	v_cvt_pk_bf16_f32 v99, v116, v117
	v_cvt_pk_bf16_f32 v100, v122, v123
	v_cvt_pk_bf16_f32 v101, v120, v121
; __device__ __forceinline__ unsigned pk_bf16(float lo, float hi) { unsigned r; asm("v_cvt_pk_bf16_f32 %0, %1, %2" : "=v"(r) : "v"(lo), "v"(hi)); return r; }
;     __device__ __forceinline__ void operator()(const f32x4 (&acc)[2][2][4][2], const pg8::Unit& u, int wr, int wc, int fr_, int fq_, const LAS uchar* bl) const {
;     ...
;                 for (int m = 0; m < 4; ++m) { const int t = row0 + ai * 128 + m * 16;
;                     cs[m][0] = *(const f32x4*)(COS + (size_t)t * 128 + i0); cs[m][1] = *(const f32x4*)(COS + (size_t)t * 128 + i0 + 4); cs[m][2] = *(const f32x4*)(SIN + (size_t)t * 128 + i0); cs[m][3] = *(const f32x4*)(SIN + (size_t)t * 128 + i0 + 4); }
; #pragma unroll
;                 for (int m = 0; m < 4; ++m) { const int t = row0 + ai * 128 + m * 16; bf16* rowp = O + (size_t)(u.col0 >> 8) * PANP + (size_t)t * 256 + (col0 & 255);
;                     const f32x4 c0 = cs[m][0], c1 = cs[m][1], s0 = cs[m][2], s1 = cs[m][3];
;                     const f32x4 a0 = acc[ai][0][m][0], a1 = acc[ai][0][m][1], b0 = acc[ai][1][m][0], b1 = acc[ai][1][m][1];
;                     const f32x4 p0 = (a0 * c0 - b0 * s0) * sc, p1 = (a1 * c1 - b1 * s1) * sc, q0 = (b0 * c0 + a0 * s0) * sc, q1 = (b1 * c1 + a1 * s1) * sc;
;                     u32x4 w; w.x = pk_bf16(p0[0], p0[1]); w.y = pk_bf16(p0[2], p0[3]); w.z = pk_bf16(p1[0], p1[1]); w.w = pk_bf16(p1[2], p1[3]); *(u32x4*)rowp = w;
;                     w.x = pk_bf16(q0[0], q0[1]); w.y = pk_bf16(q0[2], q0[3]); w.z = pk_bf16(q1[0], q1[1]); w.w = pk_bf16(q1[2], q1[3]); *(u32x4*)(rowp + 128) = w; } }
	v_pk_mul_f32 v[118:119], v[202:203], v[118:119] op_sel_hi:[0,1]
	v_pk_mul_f32 v[102:103], v[202:203], v[102:103] op_sel_hi:[0,1]
	v_cvt_pk_bf16_f32 v98, v118, v119
	global_store_dwordx4 v[114:115], v[98:101], off sc1
	s_nop 1
	v_cvt_pk_bf16_f32 v99, v104, v105
	v_cvt_pk_bf16_f32 v100, v108, v109
	v_cvt_pk_bf16_f32 v101, v106, v107
	v_pk_mul_f32 v[104:105], v[84:85], v[144:145]
	v_cvt_pk_bf16_f32 v98, v102, v103
	global_store_dwordx4 v[114:115], v[98:101], off offset:256 sc1
	v_pk_mul_f32 v[102:103], v[86:87], v[158:159]
	v_pk_mul_f32 v[106:107], v[82:83], v[142:143]
	v_pk_mul_f32 v[100:101], v[88:89], v[160:161]
	v_pk_fma_f32 v[104:105], v[92:93], v[140:141], v[104:105] neg_lo:[0,0,1] neg_hi:[0,0,1]
	v_pk_mul_f32 v[92:93], v[92:93], v[144:145]
	v_lshl_add_u64 v[98:99], s[38:39], 0, v[212:213]
	v_pk_fma_f32 v[100:101], v[96:97], v[152:153], v[100:101] neg_lo:[0,0,1] neg_hi:[0,0,1]
	v_pk_fma_f32 v[102:103], v[94:95], v[150:151], v[102:103] neg_lo:[0,0,1] neg_hi:[0,0,1]
	v_pk_fma_f32 v[106:107], v[90:91], v[138:139], v[106:107] neg_lo:[0,0,1] neg_hi:[0,0,1]
	v_pk_mul_f32 v[96:97], v[96:97], v[160:161]
	v_pk_mul_f32 v[94:95], v[94:95], v[158:159]
	v_pk_mul_f32 v[90:91], v[90:91], v[142:143]
	v_pk_fma_f32 v[84:85], v[84:85], v[140:141], v[92:93]
	v_lshl_add_u64 v[98:99], v[98:99], 0, v[190:191]
	v_pk_mul_f32 v[104:105], v[202:203], v[104:105] op_sel_hi:[0,1]
	v_pk_mul_f32 v[106:107], v[202:203], v[106:107] op_sel_hi:[0,1]
	v_pk_fma_f32 v[88:89], v[88:89], v[152:153], v[96:97]
	v_pk_fma_f32 v[86:87], v[86:87], v[150:151], v[94:95]
	v_pk_fma_f32 v[82:83], v[82:83], v[138:139], v[90:91]
	v_pk_mul_f32 v[90:91], v[202:203], v[84:85] op_sel_hi:[0,1]
	v_cvt_pk_bf16_f32 v84, v106, v107
	v_cvt_pk_bf16_f32 v85, v104, v105
	v_pk_mul_f32 v[100:101], v[202:203], v[100:101] op_sel_hi:[0,1]
	v_pk_mul_f32 v[102:103], v[202:203], v[102:103] op_sel_hi:[0,1]
	v_pk_mul_f32 v[88:89], v[202:203], v[88:89] op_sel_hi:[0,1]
	v_pk_mul_f32 v[86:87], v[202:203], v[86:87] op_sel_hi:[0,1]
	v_pk_mul_f32 v[92:93], v[202:203], v[82:83] op_sel_hi:[0,1]
	v_cvt_pk_bf16_f32 v82, v102, v103
	v_cvt_pk_bf16_f32 v83, v100, v101
	global_store_dwordx4 v[98:99], v[82:85], off sc1
	s_nop 1
	v_cvt_pk_bf16_f32 v84, v92, v93
	v_cvt_pk_bf16_f32 v85, v90, v91
	v_pk_mul_f32 v[90:91], v[66:67], v[154:155]
	v_cvt_pk_bf16_f32 v82, v86, v87
	v_cvt_pk_bf16_f32 v83, v88, v89
	global_store_dwordx4 v[98:99], v[82:85], off offset:256 sc1
	v_pk_mul_f32 v[86:87], v[70:71], v[166:167]
	v_pk_mul_f32 v[88:89], v[68:69], v[156:157]
	v_pk_mul_f32 v[84:85], v[72:73], v[168:169]
	v_pk_fma_f32 v[90:91], v[74:75], v[130:131], v[90:91] neg_lo:[0,0,1] neg_hi:[0,0,1]
	v_pk_mul_f32 v[74:75], v[74:75], v[154:155]
	v_lshl_add_u64 v[82:83], s[38:39], 0, v[210:211]
	v_pk_fma_f32 v[84:85], v[80:81], v[136:137], v[84:85] neg_lo:[0,0,1] neg_hi:[0,0,1]
	v_pk_fma_f32 v[86:87], v[78:79], v[134:135], v[86:87] neg_lo:[0,0,1] neg_hi:[0,0,1]
	v_pk_fma_f32 v[88:89], v[76:77], v[132:133], v[88:89] neg_lo:[0,0,1] neg_hi:[0,0,1]
	v_pk_mul_f32 v[80:81], v[80:81], v[168:169]
	v_pk_mul_f32 v[78:79], v[78:79], v[166:167]
	v_pk_mul_f32 v[76:77], v[76:77], v[156:157]
	v_pk_fma_f32 v[66:67], v[66:67], v[130:131], v[74:75]
	v_lshl_add_u64 v[82:83], v[82:83], 0, v[190:191]
	v_pk_mul_f32 v[84:85], v[202:203], v[84:85] op_sel_hi:[0,1]
	v_pk_mul_f32 v[86:87], v[202:203], v[86:87] op_sel_hi:[0,1]
	v_pk_fma_f32 v[72:73], v[72:73], v[136:137], v[80:81]
	v_pk_fma_f32 v[70:71], v[70:71], v[134:135], v[78:79]
	v_pk_fma_f32 v[68:69], v[68:69], v[132:133], v[76:77]
	v_pk_mul_f32 v[76:77], v[202:203], v[66:67] op_sel_hi:[0,1]
	v_cvt_pk_bf16_f32 v66, v86, v87
	v_cvt_pk_bf16_f32 v67, v84, v85
	v_pk_mul_f32 v[88:89], v[202:203], v[88:89] op_sel_hi:[0,1]
	v_pk_mul_f32 v[90:91], v[202:203], v[90:91] op_sel_hi:[0,1]
	v_pk_mul_f32 v[72:73], v[202:203], v[72:73] op_sel_hi:[0,1]
	v_pk_mul_f32 v[70:71], v[202:203], v[70:71] op_sel_hi:[0,1]
	v_pk_mul_f32 v[74:75], v[202:203], v[68:69] op_sel_hi:[0,1]
	v_cvt_pk_bf16_f32 v68, v90, v91
	v_cvt_pk_bf16_f32 v69, v88, v89
	global_store_dwordx4 v[82:83], v[66:69], off sc1
	v_lshl_add_u64 v[130:131], v[208:209], 0, s[24:25]
	v_lshl_add_u64 v[132:133], v[208:209], 0, s[26:27]
	v_cvt_pk_bf16_f32 v66, v70, v71
	v_cvt_pk_bf16_f32 v67, v72, v73
	v_cvt_pk_bf16_f32 v68, v76, v77
	v_cvt_pk_bf16_f32 v69, v74, v75
	global_store_dwordx4 v[82:83], v[66:69], off offset:256 sc1
	v_lshl_add_u64 v[134:135], v[208:209], 0, s[28:29]
	v_lshl_add_u64 v[136:137], v[208:209], 0, s[30:31]
	v_lshl_add_u64 v[66:67], v[204:205], 0, v[130:131]
	global_load_dwordx4 v[82:85], v[66:67], off offset:16
	global_load_dwordx4 v[86:89], v[66:67], off
	v_lshl_add_u64 v[66:67], v[206:207], 0, v[130:131]
	global_load_dwordx4 v[90:93], v[66:67], off offset:16
	global_load_dwordx4 v[94:97], v[66:67], off
	v_lshl_add_u64 v[66:67], v[204:205], 0, v[132:133]
	global_load_dwordx4 v[98:101], v[66:67], off offset:16
	global_load_dwordx4 v[102:105], v[66:67], off
	v_lshl_add_u64 v[66:67], v[206:207], 0, v[132:133]
	global_load_dwordx4 v[106:109], v[66:67], off offset:16
	global_load_dwordx4 v[110:113], v[66:67], off
	v_lshl_add_u64 v[66:67], v[204:205], 0, v[134:135]
	global_load_dwordx4 v[114:117], v[66:67], off offset:16
	global_load_dwordx4 v[118:121], v[66:67], off
	v_lshl_add_u64 v[66:67], v[206:207], 0, v[134:135]
	global_load_dwordx4 v[122:125], v[66:67], off offset:16
	global_load_dwordx4 v[126:129], v[66:67], off
	v_lshl_add_u64 v[70:71], v[204:205], 0, v[136:137]
	v_lshl_add_u64 v[78:79], v[206:207], 0, v[136:137]
	global_load_dwordx4 v[66:69], v[70:71], off offset:16
	global_load_dwordx4 v[74:77], v[70:71], off
	s_nop 0
	global_load_dwordx4 v[70:73], v[78:79], off offset:16
	s_nop 0
	global_load_dwordx4 v[78:81], v[78:79], off
	v_lshl_add_u64 v[130:131], s[38:39], 0, v[130:131]
	v_lshl_add_u64 v[130:131], v[130:131], 0, v[190:191]
	s_waitcnt vmcnt(13)
; __device__ __forceinline__ unsigned pk_bf16(float lo, float hi) { unsigned r; asm("v_cvt_pk_bf16_f32 %0, %1, %2" : "=v"(r) : "v"(lo), "v"(hi)); return r; }
;     __device__ __forceinline__ void operator()(const f32x4 (&acc)[2][2][4][2], const pg8::Unit& u, int wr, int wc, int fr_, int fq_, const LAS uchar* bl) const {
;     ...
;                 for (int m = 0; m < 4; ++m) { const int t = row0 + ai * 128 + m * 16;
;                     cs[m][0] = *(const f32x4*)(COS + (size_t)t * 128 + i0); cs[m][1] = *(const f32x4*)(COS + (size_t)t * 128 + i0 + 4); cs[m][2] = *(const f32x4*)(SIN + (size_t)t * 128 + i0); cs[m][3] = *(const f32x4*)(SIN + (size_t)t * 128 + i0 + 4); }
; #pragma unroll
;                 for (int m = 0; m < 4; ++m) { const int t = row0 + ai * 128 + m * 16; bf16* rowp = O + (size_t)(u.col0 >> 8) * PANP + (size_t)t * 256 + (col0 & 255);
;                     const f32x4 c0 = cs[m][0], c1 = cs[m][1], s0 = cs[m][2], s1 = cs[m][3];
;                     const f32x4 a0 = acc[ai][0][m][0], a1 = acc[ai][0][m][1], b0 = acc[ai][1][m][0], b1 = acc[ai][1][m][1];
;                     const f32x4 p0 = (a0 * c0 - b0 * s0) * sc, p1 = (a1 * c1 - b1 * s1) * sc, q0 = (b0 * c0 + a0 * s0) * sc, q1 = (b1 * c1 + a1 * s1) * sc;
;                     u32x4 w; w.x = pk_bf16(p0[0], p0[1]); w.y = pk_bf16(p0[2], p0[3]); w.z = pk_bf16(p1[0], p1[1]); w.w = pk_bf16(p1[2], p1[3]); *(u32x4*)rowp = w;
;                     w.x = pk_bf16(q0[0], q0[1]); w.y = pk_bf16(q0[2], q0[3]); w.z = pk_bf16(q1[0], q1[1]); w.w = pk_bf16(q1[2], q1[3]); *(u32x4*)(rowp + 128) = w; } }
	v_pk_mul_f32 v[142:143], v[52:53], v[92:93]
	s_waitcnt vmcnt(12)
	v_pk_mul_f32 v[138:139], v[56:57], v[96:97]
	v_pk_mul_f32 v[144:145], v[50:51], v[90:91]
	v_pk_mul_f32 v[140:141], v[54:55], v[94:95]
	v_pk_fma_f32 v[138:139], v[64:65], v[88:89], v[138:139] neg_lo:[0,0,1] neg_hi:[0,0,1]
	v_pk_fma_f32 v[142:143], v[60:61], v[84:85], v[142:143] neg_lo:[0,0,1] neg_hi:[0,0,1]
	v_pk_fma_f32 v[144:145], v[58:59], v[82:83], v[144:145] neg_lo:[0,0,1] neg_hi:[0,0,1]
	v_pk_mul_f32 v[64:65], v[64:65], v[96:97]
	v_pk_mul_f32 v[60:61], v[60:61], v[92:93]
	v_pk_mul_f32 v[58:59], v[58:59], v[90:91]
	v_pk_fma_f32 v[140:141], v[62:63], v[86:87], v[140:141] neg_lo:[0,0,1] neg_hi:[0,0,1]
	v_pk_mul_f32 v[62:63], v[62:63], v[94:95]
	v_pk_fma_f32 v[56:57], v[56:57], v[88:89], v[64:65]
	v_pk_fma_f32 v[52:53], v[52:53], v[84:85], v[60:61]
	v_pk_fma_f32 v[50:51], v[50:51], v[82:83], v[58:59]
	v_pk_mul_f32 v[138:139], v[202:203], v[138:139] op_sel_hi:[0,1]
	v_pk_mul_f32 v[142:143], v[202:203], v[142:143] op_sel_hi:[0,1]
	v_pk_mul_f32 v[144:145], v[202:203], v[144:145] op_sel_hi:[0,1]
	v_pk_fma_f32 v[54:55], v[54:55], v[86:87], v[62:63]
	v_pk_mul_f32 v[56:57], v[202:203], v[56:57] op_sel_hi:[0,1]
	v_pk_mul_f32 v[58:59], v[202:203], v[52:53] op_sel_hi:[0,1]
	v_pk_mul_f32 v[60:61], v[202:203], v[50:51] op_sel_hi:[0,1]
	v_cvt_pk_bf16_f32 v51, v138, v139
	v_cvt_pk_bf16_f32 v52, v144, v145
	v_cvt_pk_bf16_f32 v53, v142, v143
	v_pk_mul_f32 v[140:141], v[202:203], v[140:141] op_sel_hi:[0,1]
	v_pk_mul_f32 v[54:55], v[202:203], v[54:55] op_sel_hi:[0,1]
	v_cvt_pk_bf16_f32 v50, v140, v141
	global_store_dwordx4 v[130:131], v[50:53], off sc1
	s_nop 1
	v_cvt_pk_bf16_f32 v51, v56, v57
	v_cvt_pk_bf16_f32 v52, v60, v61
	v_cvt_pk_bf16_f32 v53, v58, v59
	s_waitcnt vmcnt(10)
	v_pk_mul_f32 v[56:57], v[36:37], v[108:109]
	v_cvt_pk_bf16_f32 v50, v54, v55
	global_store_dwordx4 v[130:131], v[50:53], off offset:256 sc1
	s_waitcnt vmcnt(10)
	v_pk_mul_f32 v[54:55], v[38:39], v[110:111]
	v_pk_mul_f32 v[58:59], v[34:35], v[106:107]
	v_pk_mul_f32 v[52:53], v[40:41], v[112:113]
	v_pk_fma_f32 v[56:57], v[44:45], v[100:101], v[56:57] neg_lo:[0,0,1] neg_hi:[0,0,1]
	v_pk_mul_f32 v[44:45], v[44:45], v[108:109]
	v_lshl_add_u64 v[50:51], s[38:39], 0, v[132:133]
	v_pk_fma_f32 v[52:53], v[48:49], v[104:105], v[52:53] neg_lo:[0,0,1] neg_hi:[0,0,1]
	v_pk_fma_f32 v[54:55], v[46:47], v[102:103], v[54:55] neg_lo:[0,0,1] neg_hi:[0,0,1]
	v_pk_fma_f32 v[58:59], v[42:43], v[98:99], v[58:59] neg_lo:[0,0,1] neg_hi:[0,0,1]
	v_pk_mul_f32 v[48:49], v[48:49], v[112:113]
	v_pk_mul_f32 v[46:47], v[46:47], v[110:111]
	v_pk_mul_f32 v[42:43], v[42:43], v[106:107]
	v_pk_fma_f32 v[36:37], v[36:37], v[100:101], v[44:45]
	v_lshl_add_u64 v[50:51], v[50:51], 0, v[190:191]
	v_pk_mul_f32 v[56:57], v[202:203], v[56:57] op_sel_hi:[0,1]
	v_pk_mul_f32 v[58:59], v[202:203], v[58:59] op_sel_hi:[0,1]
	v_pk_fma_f32 v[40:41], v[40:41], v[104:105], v[48:49]
	v_pk_fma_f32 v[38:39], v[38:39], v[102:103], v[46:47]
	v_pk_fma_f32 v[34:35], v[34:35], v[98:99], v[42:43]
	v_pk_mul_f32 v[42:43], v[202:203], v[36:37] op_sel_hi:[0,1]
	v_cvt_pk_bf16_f32 v36, v58, v59
	v_cvt_pk_bf16_f32 v37, v56, v57
	v_pk_mul_f32 v[52:53], v[202:203], v[52:53] op_sel_hi:[0,1]
	v_pk_mul_f32 v[54:55], v[202:203], v[54:55] op_sel_hi:[0,1]
	v_pk_mul_f32 v[40:41], v[202:203], v[40:41] op_sel_hi:[0,1]
	v_pk_mul_f32 v[38:39], v[202:203], v[38:39] op_sel_hi:[0,1]
	v_pk_mul_f32 v[44:45], v[202:203], v[34:35] op_sel_hi:[0,1]
	v_cvt_pk_bf16_f32 v34, v54, v55
	v_cvt_pk_bf16_f32 v35, v52, v53
	global_store_dwordx4 v[50:51], v[34:37], off sc1
	s_nop 1
	v_cvt_pk_bf16_f32 v36, v44, v45
	v_cvt_pk_bf16_f32 v37, v42, v43
	s_waitcnt vmcnt(8)
	v_pk_mul_f32 v[42:43], v[18:19], v[122:123]
	v_cvt_pk_bf16_f32 v34, v38, v39
	v_cvt_pk_bf16_f32 v35, v40, v41
	global_store_dwordx4 v[50:51], v[34:37], off offset:256 sc1
	s_waitcnt vmcnt(8)
; __device__ __forceinline__ unsigned pk_bf16(float lo, float hi) { unsigned r; asm("v_cvt_pk_bf16_f32 %0, %1, %2" : "=v"(r) : "v"(lo), "v"(hi)); return r; }
;     __device__ __forceinline__ void operator()(const f32x4 (&acc)[2][2][4][2], const pg8::Unit& u, int wr, int wc, int fr_, int fq_, const LAS uchar* bl) const {
;     ...
;                 for (int m = 0; m < 4; ++m) { const int t = row0 + ai * 128 + m * 16;
;                     cs[m][0] = *(const f32x4*)(COS + (size_t)t * 128 + i0); cs[m][1] = *(const f32x4*)(COS + (size_t)t * 128 + i0 + 4); cs[m][2] = *(const f32x4*)(SIN + (size_t)t * 128 + i0); cs[m][3] = *(const f32x4*)(SIN + (size_t)t * 128 + i0 + 4); }
; #pragma unroll
;                 for (int m = 0; m < 4; ++m) { const int t = row0 + ai * 128 + m * 16; bf16* rowp = O + (size_t)(u.col0 >> 8) * PANP + (size_t)t * 256 + (col0 & 255);
;                     const f32x4 c0 = cs[m][0], c1 = cs[m][1], s0 = cs[m][2], s1 = cs[m][3];
;                     const f32x4 a0 = acc[ai][0][m][0], a1 = acc[ai][0][m][1], b0 = acc[ai][1][m][0], b1 = acc[ai][1][m][1];
;                     const f32x4 p0 = (a0 * c0 - b0 * s0) * sc, p1 = (a1 * c1 - b1 * s1) * sc, q0 = (b0 * c0 + a0 * s0) * sc, q1 = (b1 * c1 + a1 * s1) * sc;
;                     u32x4 w; w.x = pk_bf16(p0[0], p0[1]); w.y = pk_bf16(p0[2], p0[3]); w.z = pk_bf16(p1[0], p1[1]); w.w = pk_bf16(p1[2], p1[3]); *(u32x4*)rowp = w;
;                     w.x = pk_bf16(q0[0], q0[1]); w.y = pk_bf16(q0[2], q0[3]); w.z = pk_bf16(q1[0], q1[1]); w.w = pk_bf16(q1[2], q1[3]); *(u32x4*)(rowp + 128) = w; } }
	v_pk_mul_f32 v[38:39], v[22:23], v[126:127]
	v_pk_mul_f32 v[40:41], v[20:21], v[124:125]
	v_pk_mul_f32 v[36:37], v[24:25], v[128:129]
	v_pk_fma_f32 v[42:43], v[26:27], v[114:115], v[42:43] neg_lo:[0,0,1] neg_hi:[0,0,1]
	v_pk_mul_f32 v[26:27], v[26:27], v[122:123]
	v_lshl_add_u64 v[34:35], s[38:39], 0, v[134:135]
	v_pk_fma_f32 v[36:37], v[32:33], v[120:121], v[36:37] neg_lo:[0,0,1] neg_hi:[0,0,1]
	v_pk_fma_f32 v[38:39], v[30:31], v[118:119], v[38:39] neg_lo:[0,0,1] neg_hi:[0,0,1]
	v_pk_fma_f32 v[40:41], v[28:29], v[116:117], v[40:41] neg_lo:[0,0,1] neg_hi:[0,0,1]
	v_pk_mul_f32 v[32:33], v[32:33], v[128:129]
	v_pk_mul_f32 v[30:31], v[30:31], v[126:127]
	v_pk_mul_f32 v[28:29], v[28:29], v[124:125]
	v_pk_fma_f32 v[18:19], v[18:19], v[114:115], v[26:27]
	v_lshl_add_u64 v[34:35], v[34:35], 0, v[190:191]
	v_pk_mul_f32 v[36:37], v[202:203], v[36:37] op_sel_hi:[0,1]
	v_pk_mul_f32 v[38:39], v[202:203], v[38:39] op_sel_hi:[0,1]
	v_pk_fma_f32 v[24:25], v[24:25], v[120:121], v[32:33]
	v_pk_fma_f32 v[22:23], v[22:23], v[118:119], v[30:31]
	v_pk_fma_f32 v[20:21], v[20:21], v[116:117], v[28:29]
	v_pk_mul_f32 v[28:29], v[202:203], v[18:19] op_sel_hi:[0,1]
	v_cvt_pk_bf16_f32 v18, v38, v39
	v_cvt_pk_bf16_f32 v19, v36, v37
	v_pk_mul_f32 v[40:41], v[202:203], v[40:41] op_sel_hi:[0,1]
	v_pk_mul_f32 v[42:43], v[202:203], v[42:43] op_sel_hi:[0,1]
	v_pk_mul_f32 v[24:25], v[202:203], v[24:25] op_sel_hi:[0,1]
	v_pk_mul_f32 v[22:23], v[202:203], v[22:23] op_sel_hi:[0,1]
	v_pk_mul_f32 v[26:27], v[202:203], v[20:21] op_sel_hi:[0,1]
	v_cvt_pk_bf16_f32 v20, v42, v43
	v_cvt_pk_bf16_f32 v21, v40, v41
	global_store_dwordx4 v[34:35], v[18:21], off sc1
	s_nop 1
	v_cvt_pk_bf16_f32 v18, v22, v23
	v_cvt_pk_bf16_f32 v19, v24, v25
	v_cvt_pk_bf16_f32 v20, v28, v29
	v_cvt_pk_bf16_f32 v21, v26, v27
	global_store_dwordx4 v[34:35], v[18:21], off offset:256 sc1
	s_waitcnt vmcnt(7)
	v_pk_mul_f32 v[22:23], v[4:5], v[72:73]
	v_pk_mul_f32 v[24:25], v[2:3], v[70:71]
	v_lshl_add_u64 v[18:19], s[38:39], 0, v[136:137]
	v_lshl_add_u64 v[136:137], v[18:19], 0, v[190:191]
	s_waitcnt vmcnt(6)
	v_pk_mul_f32 v[18:19], v[8:9], v[80:81]
	v_pk_mul_f32 v[20:21], v[6:7], v[78:79]
	v_pk_fma_f32 v[18:19], v[16:17], v[76:77], v[18:19] neg_lo:[0,0,1] neg_hi:[0,0,1]
	v_pk_fma_f32 v[20:21], v[14:15], v[74:75], v[20:21] neg_lo:[0,0,1] neg_hi:[0,0,1]
	v_pk_fma_f32 v[22:23], v[12:13], v[68:69], v[22:23] neg_lo:[0,0,1] neg_hi:[0,0,1]
	v_pk_fma_f32 v[24:25], v[10:11], v[66:67], v[24:25] neg_lo:[0,0,1] neg_hi:[0,0,1]
	v_pk_mul_f32 v[16:17], v[16:17], v[80:81]
	v_pk_mul_f32 v[14:15], v[14:15], v[78:79]
	v_pk_mul_f32 v[12:13], v[12:13], v[72:73]
	v_pk_mul_f32 v[10:11], v[10:11], v[70:71]
	v_pk_fma_f32 v[8:9], v[8:9], v[76:77], v[16:17]
	v_pk_fma_f32 v[6:7], v[6:7], v[74:75], v[14:15]
	v_pk_fma_f32 v[4:5], v[4:5], v[68:69], v[12:13]
	v_pk_fma_f32 v[2:3], v[2:3], v[66:67], v[10:11]
	v_pk_mul_f32 v[18:19], v[202:203], v[18:19] op_sel_hi:[0,1]
	v_pk_mul_f32 v[20:21], v[202:203], v[20:21] op_sel_hi:[0,1]
	v_pk_mul_f32 v[22:23], v[202:203], v[22:23] op_sel_hi:[0,1]
	v_pk_mul_f32 v[24:25], v[202:203], v[24:25] op_sel_hi:[0,1]
	v_pk_mul_f32 v[8:9], v[202:203], v[8:9] op_sel_hi:[0,1]
	v_pk_mul_f32 v[6:7], v[202:203], v[6:7] op_sel_hi:[0,1]
	v_pk_mul_f32 v[10:11], v[202:203], v[4:5] op_sel_hi:[0,1]
	v_pk_mul_f32 v[12:13], v[202:203], v[2:3] op_sel_hi:[0,1]
	v_cvt_pk_bf16_f32 v2, v20, v21
	v_cvt_pk_bf16_f32 v3, v18, v19
	v_cvt_pk_bf16_f32 v4, v24, v25
	v_cvt_pk_bf16_f32 v5, v22, v23
	global_store_dwordx4 v[136:137], v[2:5], off sc1
	v_cvt_pk_bf16_f32 v130, v6, v7
	v_cvt_pk_bf16_f32 v131, v8, v9
	v_cvt_pk_bf16_f32 v132, v12, v13
	v_cvt_pk_bf16_f32 v133, v10, v11
	s_andn2_b64 vcc, exec, s[2:3]
	s_mov_b64 s[2:3], -1
	global_store_dwordx4 v[136:137], v[130:133], off offset:256 sc1
	s_cbranch_vccnz .LBB0_107
